# RG-LRU backward pass: gate tile fetched by LDS-DMA (2 pieces per wave) and read from LDS instead of 16 two-byte global gathers per lane per chunk
# speedup vs baseline: 1.0123x; 1.0071x over previous
.Lmylru_nw_4:
	v_or_b32_e32 v169, 0x10000, v165
	v_or_b32_e32 v170, 0x10000, v166
	v_or_b32_e32 v171, 0x10000, v167
	v_or_b32_e32 v172, 0x10000, v168
	ds_read_u16 v144, v169
	ds_read_u16 v145, v170
	ds_read_u16 v146, v171
	ds_read_u16 v147, v172
	ds_read_u16 v148, v169 offset:8192
	ds_read_u16 v149, v170 offset:8192
	ds_read_u16 v150, v171 offset:8192
	ds_read_u16 v151, v172 offset:8192
	ds_read_u16 v152, v169 offset:16384
	ds_read_u16 v153, v170 offset:16384
	ds_read_u16 v154, v171 offset:16384
	ds_read_u16 v155, v172 offset:16384
	ds_read_u16 v156, v169 offset:24576
	ds_read_u16 v157, v170 offset:24576
	ds_read_u16 v158, v171 offset:24576
	ds_read_u16 v159, v172 offset:24576
	s_nop 7
	v_fma_f32 v178, v64, s53, v173
	v_fma_f32 v179, v65, s53, v173
	v_fma_f32 v180, v66, s53, v173
	v_fma_f32 v181, v67, s53, v173
	v_fma_f32 v182, v72, s53, v173
	v_fma_f32 v183, v73, s53, v173
	v_fma_f32 v184, v74, s53, v173
	v_fma_f32 v185, v75, s53, v173
	v_fma_f32 v186, v68, s53, v174
	v_fma_f32 v187, v69, s53, v174
	v_fma_f32 v188, v70, s53, v174
	v_fma_f32 v189, v71, s53, v174
	v_fma_f32 v190, v76, s53, v174
	v_fma_f32 v191, v77, s53, v174
	v_fma_f32 v192, v78, s53, v174
	v_fma_f32 v193, v79, s53, v174
	v_exp_f32_e32 v178, v178
	v_exp_f32_e32 v179, v179
	v_exp_f32_e32 v180, v180
	v_exp_f32_e32 v181, v181
	v_exp_f32_e32 v182, v182
	v_exp_f32_e32 v183, v183
	v_exp_f32_e32 v184, v184
	v_exp_f32_e32 v185, v185
	v_exp_f32_e32 v186, v186
	v_exp_f32_e32 v187, v187
	v_exp_f32_e32 v188, v188
	v_exp_f32_e32 v189, v189
	v_exp_f32_e32 v190, v190
	v_exp_f32_e32 v191, v191
	v_exp_f32_e32 v192, v192
	v_exp_f32_e32 v193, v193
	v_add_f32_e32 v178, 1.0, v178
	v_add_f32_e32 v179, 1.0, v179
	v_add_f32_e32 v180, 1.0, v180
	v_add_f32_e32 v181, 1.0, v181
	v_add_f32_e32 v182, 1.0, v182
	v_add_f32_e32 v183, 1.0, v183
	v_add_f32_e32 v184, 1.0, v184
	v_add_f32_e32 v185, 1.0, v185
	v_add_f32_e32 v186, 1.0, v186
	v_add_f32_e32 v187, 1.0, v187
	v_add_f32_e32 v188, 1.0, v188
	v_add_f32_e32 v189, 1.0, v189
	v_add_f32_e32 v190, 1.0, v190
	v_add_f32_e32 v191, 1.0, v191
	v_add_f32_e32 v192, 1.0, v192
	v_add_f32_e32 v193, 1.0, v193
	v_rcp_f32_e32 v178, v178
	v_rcp_f32_e32 v179, v179
	v_rcp_f32_e32 v180, v180
	v_rcp_f32_e32 v181, v181
	v_rcp_f32_e32 v182, v182
	v_rcp_f32_e32 v183, v183
	v_rcp_f32_e32 v184, v184
	v_rcp_f32_e32 v185, v185
	v_rcp_f32_e32 v186, v186
	v_rcp_f32_e32 v187, v187
	v_rcp_f32_e32 v188, v188
	v_rcp_f32_e32 v189, v189
	v_rcp_f32_e32 v190, v190
	v_rcp_f32_e32 v191, v191
	v_rcp_f32_e32 v192, v192
	v_rcp_f32_e32 v193, v193
	v_mul_f32_e32 v178, v175, v178
	v_mul_f32_e32 v179, v175, v179
	v_mul_f32_e32 v180, v175, v180
	v_mul_f32_e32 v181, v175, v181
	v_mul_f32_e32 v182, v175, v182
	v_mul_f32_e32 v183, v175, v183
	v_mul_f32_e32 v184, v175, v184
	v_mul_f32_e32 v185, v175, v185
	v_exp_f32_e32 v96, v178
	v_exp_f32_e32 v97, v179
	v_exp_f32_e32 v98, v180
	v_exp_f32_e32 v99, v181
	v_exp_f32_e32 v100, v182
	v_exp_f32_e32 v101, v183
	v_exp_f32_e32 v102, v184
	v_exp_f32_e32 v103, v185
	s_nop 0
	v_fma_f32 v194, -v96, v96, 1.0
	v_fma_f32 v195, -v97, v97, 1.0
	v_fma_f32 v196, -v98, v98, 1.0
	v_fma_f32 v197, -v99, v99, 1.0
	v_fma_f32 v198, -v100, v100, 1.0
	v_fma_f32 v199, -v101, v101, 1.0
	v_fma_f32 v200, -v102, v102, 1.0
	v_fma_f32 v201, -v103, v103, 1.0
	v_max_f32_e32 v194, 0, v194
	v_max_f32_e32 v195, 0, v195
	v_max_f32_e32 v196, 0, v196
	v_max_f32_e32 v197, 0, v197
	v_max_f32_e32 v198, 0, v198
	v_max_f32_e32 v199, 0, v199
	v_max_f32_e32 v200, 0, v200
	v_max_f32_e32 v201, 0, v201
	v_sqrt_f32_e32 v194, v194
	v_sqrt_f32_e32 v195, v195
	v_sqrt_f32_e32 v196, v196
	v_sqrt_f32_e32 v197, v197
	v_sqrt_f32_e32 v198, v198
	v_sqrt_f32_e32 v199, v199
	v_sqrt_f32_e32 v200, v200
	v_sqrt_f32_e32 v201, v201
	s_waitcnt lgkmcnt(8)
	v_lshlrev_b32_e32 v144, 16, v144
	v_lshlrev_b32_e32 v145, 16, v145
	v_lshlrev_b32_e32 v146, 16, v146
	v_lshlrev_b32_e32 v147, 16, v147
	v_lshlrev_b32_e32 v148, 16, v148
	v_lshlrev_b32_e32 v149, 16, v149
	v_lshlrev_b32_e32 v150, 16, v150
	v_lshlrev_b32_e32 v151, 16, v151
	v_mul_f32_e32 v194, v194, v186
	v_mul_f32_e32 v195, v195, v187
	v_mul_f32_e32 v196, v196, v188
	v_mul_f32_e32 v197, v197, v189
	v_mul_f32_e32 v198, v198, v190
	v_mul_f32_e32 v199, v199, v191
	v_mul_f32_e32 v200, v200, v192
	v_mul_f32_e32 v201, v201, v193
	v_mul_f32_e32 v144, v194, v144
	v_mul_f32_e32 v145, v195, v145
	v_mul_f32_e32 v146, v196, v146
	v_mul_f32_e32 v147, v197, v147
	v_mul_f32_e32 v148, v198, v148
	v_mul_f32_e32 v149, v199, v149
	v_mul_f32_e32 v150, v200, v150
	v_mul_f32_e32 v151, v201, v151
	v_fma_f32 v178, v80, s53, v173
	v_fma_f32 v179, v81, s53, v173
	v_fma_f32 v180, v82, s53, v173
	v_fma_f32 v181, v83, s53, v173
	v_fma_f32 v182, v88, s53, v173
	v_fma_f32 v183, v89, s53, v173
	v_fma_f32 v184, v90, s53, v173
	v_fma_f32 v185, v91, s53, v173
	v_fma_f32 v186, v84, s53, v174
	v_fma_f32 v187, v85, s53, v174
	v_fma_f32 v188, v86, s53, v174
	v_fma_f32 v189, v87, s53, v174
	v_fma_f32 v190, v92, s53, v174
	v_fma_f32 v191, v93, s53, v174
	v_fma_f32 v192, v94, s53, v174
	v_fma_f32 v193, v95, s53, v174
	v_exp_f32_e32 v178, v178
	v_exp_f32_e32 v179, v179
	v_exp_f32_e32 v180, v180
	v_exp_f32_e32 v181, v181
	v_exp_f32_e32 v182, v182
	v_exp_f32_e32 v183, v183
	v_exp_f32_e32 v184, v184
	v_exp_f32_e32 v185, v185
	v_exp_f32_e32 v186, v186
	v_exp_f32_e32 v187, v187
	v_exp_f32_e32 v188, v188
	v_exp_f32_e32 v189, v189
	v_exp_f32_e32 v190, v190
	v_exp_f32_e32 v191, v191
	v_exp_f32_e32 v192, v192
	v_exp_f32_e32 v193, v193
	v_add_f32_e32 v178, 1.0, v178
	v_add_f32_e32 v179, 1.0, v179
	v_add_f32_e32 v180, 1.0, v180
	v_add_f32_e32 v181, 1.0, v181
	v_add_f32_e32 v182, 1.0, v182
	v_add_f32_e32 v183, 1.0, v183
	v_add_f32_e32 v184, 1.0, v184
	v_add_f32_e32 v185, 1.0, v185
	v_add_f32_e32 v186, 1.0, v186
	v_add_f32_e32 v187, 1.0, v187
	v_add_f32_e32 v188, 1.0, v188
	v_add_f32_e32 v189, 1.0, v189
	v_add_f32_e32 v190, 1.0, v190
	v_add_f32_e32 v191, 1.0, v191
	v_add_f32_e32 v192, 1.0, v192
	v_add_f32_e32 v193, 1.0, v193
	v_rcp_f32_e32 v178, v178
	v_rcp_f32_e32 v179, v179
	v_rcp_f32_e32 v180, v180
	v_rcp_f32_e32 v181, v181
	v_rcp_f32_e32 v182, v182
	v_rcp_f32_e32 v183, v183
	v_rcp_f32_e32 v184, v184
	v_rcp_f32_e32 v185, v185
	v_rcp_f32_e32 v186, v186
	v_rcp_f32_e32 v187, v187
	v_rcp_f32_e32 v188, v188
	v_rcp_f32_e32 v189, v189
	v_rcp_f32_e32 v190, v190
	v_rcp_f32_e32 v191, v191
	v_rcp_f32_e32 v192, v192
	v_rcp_f32_e32 v193, v193
	v_mul_f32_e32 v178, v175, v178
	v_mul_f32_e32 v179, v175, v179
	v_mul_f32_e32 v180, v175, v180
	v_mul_f32_e32 v181, v175, v181
	v_mul_f32_e32 v182, v175, v182
	v_mul_f32_e32 v183, v175, v183
	v_mul_f32_e32 v184, v175, v184
	v_mul_f32_e32 v185, v175, v185
	v_exp_f32_e32 v104, v178
	v_exp_f32_e32 v105, v179
	v_exp_f32_e32 v106, v180
	v_exp_f32_e32 v107, v181
	v_exp_f32_e32 v108, v182
	v_exp_f32_e32 v109, v183
	v_exp_f32_e32 v110, v184
	v_exp_f32_e32 v111, v185
	s_nop 0
	v_fma_f32 v194, -v104, v104, 1.0
	v_fma_f32 v195, -v105, v105, 1.0
	v_fma_f32 v196, -v106, v106, 1.0
	v_fma_f32 v197, -v107, v107, 1.0
	v_fma_f32 v198, -v108, v108, 1.0
	v_fma_f32 v199, -v109, v109, 1.0
	v_fma_f32 v200, -v110, v110, 1.0
	v_fma_f32 v201, -v111, v111, 1.0
	v_max_f32_e32 v194, 0, v194
	v_max_f32_e32 v195, 0, v195
	v_max_f32_e32 v196, 0, v196
	v_max_f32_e32 v197, 0, v197
	v_max_f32_e32 v198, 0, v198
	v_max_f32_e32 v199, 0, v199
	v_max_f32_e32 v200, 0, v200
	v_max_f32_e32 v201, 0, v201
	v_sqrt_f32_e32 v194, v194
	v_sqrt_f32_e32 v195, v195
	v_sqrt_f32_e32 v196, v196
	v_sqrt_f32_e32 v197, v197
	v_sqrt_f32_e32 v198, v198
	v_sqrt_f32_e32 v199, v199
	v_sqrt_f32_e32 v200, v200
	v_sqrt_f32_e32 v201, v201
	s_waitcnt lgkmcnt(0)
	v_lshlrev_b32_e32 v152, 16, v152
	v_lshlrev_b32_e32 v153, 16, v153
	v_lshlrev_b32_e32 v154, 16, v154
	v_lshlrev_b32_e32 v155, 16, v155
	v_lshlrev_b32_e32 v156, 16, v156
	v_lshlrev_b32_e32 v157, 16, v157
	v_lshlrev_b32_e32 v158, 16, v158
	v_lshlrev_b32_e32 v159, 16, v159
	v_mul_f32_e32 v194, v194, v186
	v_mul_f32_e32 v195, v195, v187
	v_mul_f32_e32 v196, v196, v188
	v_mul_f32_e32 v197, v197, v189
	v_mul_f32_e32 v198, v198, v190
	v_mul_f32_e32 v199, v199, v191
	v_mul_f32_e32 v200, v200, v192
	v_mul_f32_e32 v201, v201, v193
	v_mul_f32_e32 v152, v194, v152
	v_mul_f32_e32 v153, v195, v153
	v_mul_f32_e32 v154, v196, v154
	v_mul_f32_e32 v155, v197, v155
	v_mul_f32_e32 v156, v198, v156
	v_mul_f32_e32 v157, v199, v157
	v_mul_f32_e32 v158, v200, v158
	v_mul_f32_e32 v159, v201, v159
	v_fma_f32 v145, v97, v144, v145
	v_fma_f32 v149, v101, v148, v149
	v_fma_f32 v153, v105, v152, v153
	v_fma_f32 v157, v109, v156, v157
	v_mul_f32_e32 v97, v97, v96
	v_mul_f32_e32 v101, v101, v100
	v_mul_f32_e32 v105, v105, v104
	v_mul_f32_e32 v109, v109, v108
	v_fma_f32 v146, v98, v145, v146
	v_fma_f32 v150, v102, v149, v150
	v_fma_f32 v154, v106, v153, v154
	v_fma_f32 v158, v110, v157, v158
	v_mul_f32_e32 v98, v98, v97
	v_mul_f32_e32 v102, v102, v101
	v_mul_f32_e32 v106, v106, v105
	v_mul_f32_e32 v110, v110, v109
	v_fma_f32 v147, v99, v146, v147
	v_fma_f32 v151, v103, v150, v151
	v_fma_f32 v155, v107, v154, v155
	v_fma_f32 v159, v111, v158, v159
	v_mul_f32_e32 v99, v99, v98
	v_mul_f32_e32 v103, v103, v102
	v_mul_f32_e32 v107, v107, v106
	v_mul_f32_e32 v111, v111, v110
	ds_bpermute_b32 v178, v204, v99
	ds_bpermute_b32 v182, v204, v147
	ds_bpermute_b32 v179, v204, v103
	ds_bpermute_b32 v183, v204, v151
	ds_bpermute_b32 v180, v204, v107
	ds_bpermute_b32 v184, v204, v155
	ds_bpermute_b32 v181, v204, v111
	ds_bpermute_b32 v185, v204, v159
	s_waitcnt lgkmcnt(0)
	v_fma_f32 v186, v182, v99, v147
	v_cndmask_b32_e64 v178, 1.0, v178, s[34:35]
	v_fma_f32 v187, v183, v103, v151
	v_cndmask_b32_e64 v179, 1.0, v179, s[34:35]
	v_fma_f32 v188, v184, v107, v155
	v_cndmask_b32_e64 v180, 1.0, v180, s[34:35]
	v_fma_f32 v189, v185, v111, v159
	v_cndmask_b32_e64 v181, 1.0, v181, s[34:35]
	v_cndmask_b32_e64 v223, v147, v186, s[34:35]
	v_mul_f32_e32 v219, v99, v178
	v_cndmask_b32_e64 v224, v151, v187, s[34:35]
	v_mul_f32_e32 v220, v103, v179
	v_cndmask_b32_e64 v225, v155, v188, s[34:35]
	v_mul_f32_e32 v221, v107, v180
	v_cndmask_b32_e64 v226, v159, v189, s[34:35]
	v_mul_f32_e32 v222, v111, v181
	ds_bpermute_b32 v178, v205, v219
	ds_bpermute_b32 v182, v205, v223
	ds_bpermute_b32 v179, v205, v220
	ds_bpermute_b32 v183, v205, v224
	ds_bpermute_b32 v180, v205, v221
	ds_bpermute_b32 v184, v205, v225
	ds_bpermute_b32 v181, v205, v222
	ds_bpermute_b32 v185, v205, v226
	s_waitcnt lgkmcnt(0)
	v_fma_f32 v186, v182, v219, v223
	v_cndmask_b32_e64 v178, 1.0, v178, s[36:37]
	v_fma_f32 v187, v183, v220, v224
	v_cndmask_b32_e64 v179, 1.0, v179, s[36:37]
	v_fma_f32 v188, v184, v221, v225
	v_cndmask_b32_e64 v180, 1.0, v180, s[36:37]
	v_fma_f32 v189, v185, v222, v226
	v_cndmask_b32_e64 v181, 1.0, v181, s[36:37]
	v_cndmask_b32_e64 v223, v223, v186, s[36:37]
	v_mul_f32_e32 v219, v219, v178
	v_cndmask_b32_e64 v224, v224, v187, s[36:37]
	v_mul_f32_e32 v220, v220, v179
	v_cndmask_b32_e64 v225, v225, v188, s[36:37]
	v_mul_f32_e32 v221, v221, v180
	v_cndmask_b32_e64 v226, v226, v189, s[36:37]
	v_mul_f32_e32 v222, v222, v181
	ds_bpermute_b32 v227, v204, v219
	ds_bpermute_b32 v231, v204, v223
	ds_bpermute_b32 v235, v206, v219
	ds_bpermute_b32 v239, v206, v223
	ds_bpermute_b32 v228, v204, v220
	ds_bpermute_b32 v232, v204, v224
	ds_bpermute_b32 v236, v206, v220
	ds_bpermute_b32 v244, v206, v224
	ds_bpermute_b32 v229, v204, v221
	ds_bpermute_b32 v233, v204, v225
	ds_bpermute_b32 v237, v206, v221
	ds_bpermute_b32 v245, v206, v225
	ds_bpermute_b32 v230, v204, v222
	ds_bpermute_b32 v234, v204, v226
	ds_bpermute_b32 v238, v206, v222
	ds_bpermute_b32 v246, v206, v226
	s_waitcnt lgkmcnt(0)
	v_cndmask_b32_e64 v227, 1.0, v227, s[34:35]
	v_cndmask_b32_e64 v231, 0, v231, s[34:35]
	v_cndmask_b32_e64 v228, 1.0, v228, s[34:35]
	v_cndmask_b32_e64 v232, 0, v232, s[34:35]
	v_cndmask_b32_e64 v229, 1.0, v229, s[34:35]
	v_cndmask_b32_e64 v233, 0, v233, s[34:35]
	v_cndmask_b32_e64 v230, 1.0, v230, s[34:35]
	v_cndmask_b32_e64 v234, 0, v234, s[34:35]
	v_mov_b32_e32 v190, v235
	v_mov_b32_e32 v194, v239
	v_mov_b32_e32 v198, v190
	v_mov_b32_e32 v201, v194
	v_fma_f32 v194, v194, v236, v244
	v_mul_f32_e32 v190, v190, v236
	v_mov_b32_e32 v199, v190
	v_mov_b32_e32 v177, v194
	v_fma_f32 v194, v194, v237, v245
	v_mul_f32_e32 v190, v190, v237
	v_mov_b32_e32 v200, v190
	v_mov_b32_e32 v203, v194
	v_fma_f32 v194, v194, v238, v246
	v_mul_f32_e32 v190, v190, v238
	v_mov_b32_e32 v191, v194
	ds_write_b64 v207, v[190:191] offset:1024
	s_waitcnt lgkmcnt(0)
	s_barrier
	ds_read_b64 v[178:179], v208 offset:1024
	ds_read_b64 v[180:181], v208 offset:1536
	s_waitcnt lgkmcnt(0)
	v_fma_f32 v182, v176, v178, v179
	v_cndmask_b32_e64 v183, v176, v182, s[38:39]
	v_fma_f32 v176, v182, v180, v181
	v_mov_b32_e32 v184, v183
	v_fma_f32 v185, v183, v198, v201
	v_fma_f32 v186, v183, v199, v177
	v_fma_f32 v187, v183, v200, v203
	v_fma_f32 v184, v184, v227, v231
	v_fma_f32 v185, v185, v228, v232
	v_fma_f32 v186, v186, v229, v233
	v_fma_f32 v187, v187, v230, v234
	v_fma_f32 v144, v184, v96, v144
	v_fma_f32 v148, v185, v100, v148
	v_fma_f32 v152, v186, v104, v152
	v_fma_f32 v156, v187, v108, v156
	v_fma_f32 v145, v184, v97, v145
	v_fma_f32 v149, v185, v101, v149
	v_fma_f32 v153, v186, v105, v153
	v_fma_f32 v157, v187, v109, v157
	v_fma_f32 v146, v184, v98, v146
	v_fma_f32 v150, v185, v102, v150
	v_fma_f32 v154, v186, v106, v154
	v_fma_f32 v158, v187, v110, v158
	v_fma_f32 v147, v184, v99, v147
	v_fma_f32 v151, v185, v103, v151
	v_fma_f32 v155, v186, v107, v155
	v_fma_f32 v159, v187, v111, v159
	v_cvt_pk_bf16_f32 v178, v144, v145
	v_cvt_pk_bf16_f32 v179, v146, v147
	v_cvt_pk_bf16_f32 v180, v148, v149
	v_cvt_pk_bf16_f32 v181, v150, v151
	v_cvt_pk_bf16_f32 v182, v152, v153
	v_cvt_pk_bf16_f32 v183, v154, v155
	v_cvt_pk_bf16_f32 v184, v156, v157
	v_cvt_pk_bf16_f32 v185, v158, v159
	global_store_dword v209, v178, s[44:45]
	global_store_dword v209, v179, s[44:45] offset:256
	global_store_dword v209, v180, s[44:45] offset:512
	global_store_dword v209, v181, s[44:45] offset:768
	global_store_dword v209, v182, s[44:45] offset:1024
	global_store_dword v209, v183, s[44:45] offset:1280
	global_store_dword v209, v184, s[44:45] offset:1536
	global_store_dword v209, v185, s[44:45] offset:1792
	s_add_i32 s13, s13, 1
	s_add_i32 s60, s60, -1
	s_cmp_lg_u32 s60, 0
	s_cbranch_scc1 .Lmylru_loop_0
	s_load_dwordx2 s[46:47], s[0:1], 0xc8
	s_load_dwordx2 s[48:49], s[0:1], 0xd8
	s_load_dwordx2 s[40:41], s[0:1], 0xe0
	s_lshl_b32 s50, s10, 8
	s_lshl_b32 s51, s11, 6
	s_add_i32 s50, s50, s51
	s_lshl_b32 s51, s8, 4
	s_add_i32 s50, s50, s51
	v_add_u32_e32 v179, s50, v160
	v_lshlrev_b32_e32 v179, 2, v179
	s_waitcnt lgkmcnt(0)
	global_load_dword v173, v179, s[46:47]
	global_load_dword v174, v179, s[48:49]
	global_load_dword v175, v179, s[40:41]
	v_cmp_gt_u32_e64 s[34:35], 48, v202
	v_cmp_gt_u32_e64 s[36:37], 32, v202
	v_add_u32_e32 v204, 16, v202
	v_add_u32_e32 v205, 32, v202
	v_mov_b32_e32 v206, v160
	s_cmp_eq_u32 s7, 0
	s_cselect_b64 s[38:39], -1, 0
	v_and_b32_e32 v204, 63, v204
	v_lshlrev_b32_e32 v204, 2, v204
	v_and_b32_e32 v205, 63, v205
	v_lshlrev_b32_e32 v205, 2, v205
	v_and_b32_e32 v206, 63, v206
	v_lshlrev_b32_e32 v206, 2, v206
	v_lshrrev_b32_e32 v255, 3, v202
	v_lshlrev_b32_e32 v255, 11, v255
	v_and_b32_e32 v178, 7, v202
	v_lshl_add_u32 v255, v178, 4, v255
	s_lshl_b32 s50, s6, 15
	v_add_u32_e32 v255, s50, v255
	v_mov_b32_e32 v176, 0
	s_mov_b32 s53, 0xbfb8aa3b
	s_mov_b32 s13, 0
	s_barrier
	s_cmp_lt_u32 s13, 2
	s_sub_i32 s50, 1, s13
	s_lshl_b32 s50, s50, 7
	s_lshl_b32 s51, s9, 8
	s_add_i32 s51, s51, 0x8000
	s_add_i32 s51, s51, s50
	s_sub_i32 s50, 17, s13
	s_lshl_b32 s50, s50, 7
	s_lshl_b32 s59, s9, 11
	s_add_i32 s59, s59, s50
	s_cmp_lt_u32 s13, 2
	s_cselect_b32 s59, s51, s59
	s_lshl_b32 s52, s59, 11
	s_add_u32 s46, s16, s52
	s_addc_u32 s47, s17, 0
	s_lshl_b32 s52, s6, 13
	s_mov_b32 m0, s52
	s_add_i32 s52, s52, 0x400
	global_load_lds_dwordx4 v211, s[46:47]
	s_mov_b32 m0, s52
	s_add_i32 s52, s52, 0x400
	global_load_lds_dwordx4 v212, s[46:47]
	s_mov_b32 m0, s52
	s_add_i32 s52, s52, 0x400
	global_load_lds_dwordx4 v213, s[46:47]
	s_mov_b32 m0, s52
	s_add_i32 s52, s52, 0x400
	global_load_lds_dwordx4 v214, s[46:47]
	s_mov_b32 m0, s52
	s_add_i32 s52, s52, 0x400
	global_load_lds_dwordx4 v215, s[46:47]
	s_mov_b32 m0, s52
	s_add_i32 s52, s52, 0x400
	global_load_lds_dwordx4 v216, s[46:47]
	s_mov_b32 m0, s52
	s_add_i32 s52, s52, 0x400
	global_load_lds_dwordx4 v217, s[46:47]
	s_mov_b32 m0, s52
	s_nop 0
	global_load_lds_dwordx4 v218, s[46:47]
	s_waitcnt vmcnt(8)
	v_mul_f32_e32 v173, s53, v173
	v_mul_f32_e32 v174, s53, v174
	v_mul_f32_e32 v175, s53, v175
	v_exp_f32_e32 v175, v175
	s_nop 0
	v_add_f32_e32 v180, 1.0, v175
	v_log_f32_e32 v180, v180
	v_mov_b32_e32 v181, 0x3eaaaaab
	v_fma_f32 v181, v175, v181, -0.5
	v_fma_f32 v181, v175, v181, 1.0
	v_mul_f32_e32 v181, v175, v181
	v_mul_f32_e32 v181, 0x3fb8aa3b, v181
	v_cmp_gt_f32_e32 vcc, 0x3cf5c28f, v175
	s_nop 1
	v_cndmask_b32_e32 v175, v180, v181, vcc
	v_mul_f32_e32 v175, 0xc1000000, v175
	s_waitcnt vmcnt(0)
	s_barrier
	s_cmp_eq_u32 s13, 17
	s_cbranch_scc1 .Lmylru_nodma_5
	s_add_i32 s58, s13, 1
	s_cmp_lt_u32 s58, 2
	s_sub_i32 s50, 1, s58
	s_lshl_b32 s50, s50, 7
	s_lshl_b32 s51, s9, 8
	s_add_i32 s51, s51, 0x8000
	s_add_i32 s51, s51, s50
	s_sub_i32 s50, 17, s58
	s_lshl_b32 s50, s50, 7
	s_lshl_b32 s59, s9, 11
	s_add_i32 s59, s59, s50
	s_cmp_lt_u32 s58, 2
	s_cselect_b32 s59, s51, s59
	s_lshl_b32 s52, s59, 11
	s_add_u32 s46, s16, s52
	s_addc_u32 s47, s17, 0
	s_lshl_b32 s52, s6, 13
	s_add_i32 s52, s52, 0x10000
	s_mov_b32 m0, s52
	s_add_i32 s52, s52, 0x400
	global_load_lds_dwordx4 v211, s[46:47]
	s_mov_b32 m0, s52
	s_add_i32 s52, s52, 0x400
	global_load_lds_dwordx4 v212, s[46:47]
	s_mov_b32 m0, s52
	s_add_i32 s52, s52, 0x400
	global_load_lds_dwordx4 v213, s[46:47]
	s_mov_b32 m0, s52
	s_add_i32 s52, s52, 0x400
	global_load_lds_dwordx4 v214, s[46:47]
	s_mov_b32 m0, s52
	s_add_i32 s52, s52, 0x400
	global_load_lds_dwordx4 v215, s[46:47]
	s_mov_b32 m0, s52
	s_add_i32 s52, s52, 0x400
	global_load_lds_dwordx4 v216, s[46:47]
	s_mov_b32 m0, s52
	s_add_i32 s52, s52, 0x400
	global_load_lds_dwordx4 v217, s[46:47]
	s_mov_b32 m0, s52
	s_nop 0
	global_load_lds_dwordx4 v218, s[46:47]

.Lmylru_t1_7:
	s_barrier
	s_sub_i32 s54, 17, s13
	s_lshl_b32 s55, s54, 14
	s_lshl_b32 s56, s6, 11
	s_add_i32 s55, s55, s56
	s_add_u32 s44, s22, s55
	s_addc_u32 s45, s23, 0
	s_cmp_lt_u32 s13, 2
	s_sub_i32 s50, 1, s13
	s_lshl_b32 s50, s50, 7
	s_lshl_b32 s51, s9, 8
	s_add_i32 s51, s51, 0x8000
	s_add_i32 s51, s51, s50
	s_sub_i32 s50, 17, s13
	s_lshl_b32 s50, s50, 7
	s_lshl_b32 s57, s9, 11
	s_add_i32 s57, s57, s50
	s_cmp_lt_u32 s13, 2
	s_cselect_b32 s57, s51, s57
	s_lshl_b32 s57, s57, 11
	s_add_u32 s40, s18, s57
	s_addc_u32 s41, s19, 0
	s_add_u32 s42, s20, s57
	s_addc_u32 s43, s21, 0
	global_load_dword v247, v209, s[44:45]
	global_load_dword v248, v209, s[44:45] offset:256
	global_load_dword v249, v209, s[44:45] offset:512
	global_load_dword v250, v209, s[44:45] offset:768
	global_load_dword v251, v209, s[44:45] offset:1024
	global_load_dword v252, v209, s[44:45] offset:1280
	global_load_dword v253, v209, s[44:45] offset:1536
	global_load_dword v254, v209, s[44:45] offset:1792
	s_lshl_b32 s52, s6, 11
	s_add_i32 s52, s52, 0x20800
	s_mov_b32 m0, s52
	v_add_u32_e32 v182, 0x4000, v255
	global_load_lds_dwordx4 v255, s[40:41]
	s_add_i32 s52, s52, 0x400
	s_mov_b32 m0, s52
	s_nop 0
	global_load_lds_dwordx4 v182, s[40:41]
	s_cmp_eq_u32 s13, 17
	s_cbranch_scc1 .Lmylru_nodma_7
	s_add_i32 s58, s13, 1
	s_cmp_lt_u32 s58, 2
	s_sub_i32 s50, 1, s58
	s_lshl_b32 s50, s50, 7
	s_lshl_b32 s51, s9, 8
	s_add_i32 s51, s51, 0x8000
	s_add_i32 s51, s51, s50
	s_sub_i32 s50, 17, s58
	s_lshl_b32 s50, s50, 7
	s_lshl_b32 s59, s9, 11
	s_add_i32 s59, s59, s50
	s_cmp_lt_u32 s58, 2
	s_cselect_b32 s59, s51, s59
	s_lshl_b32 s52, s59, 11
	s_add_u32 s46, s16, s52
	s_addc_u32 s47, s17, 0
	s_lshl_b32 s52, s6, 13
	s_add_i32 s52, s52, 0x10000
	s_mov_b32 m0, s52
	s_add_i32 s52, s52, 0x400
	global_load_lds_dwordx4 v211, s[46:47]
	s_mov_b32 m0, s52
	s_add_i32 s52, s52, 0x400
	global_load_lds_dwordx4 v212, s[46:47]
	s_mov_b32 m0, s52
	s_add_i32 s52, s52, 0x400
	global_load_lds_dwordx4 v213, s[46:47]
	s_mov_b32 m0, s52
	s_add_i32 s52, s52, 0x400
	global_load_lds_dwordx4 v214, s[46:47]
	s_mov_b32 m0, s52
	s_add_i32 s52, s52, 0x400
	global_load_lds_dwordx4 v215, s[46:47]
	s_mov_b32 m0, s52
	s_add_i32 s52, s52, 0x400
	global_load_lds_dwordx4 v216, s[46:47]
	s_mov_b32 m0, s52
	s_add_i32 s52, s52, 0x400
	global_load_lds_dwordx4 v217, s[46:47]
	s_mov_b32 m0, s52
	s_nop 0
	global_load_lds_dwordx4 v218, s[46:47]
.Lmylru_nodma_7:
	v_mov_b32_e32 v163, v162
	ds_read_b128 v[96:99], v163
	ds_read_b128 v[100:103], v163 offset:8192
	ds_read_b128 v[104:107], v163 offset:16384
	ds_read_b128 v[108:111], v163 offset:24576
	v_xor_b32_e32 v164, 0x40, v163
	ds_read_b128 v[112:115], v164
	ds_read_b128 v[116:119], v164 offset:8192
	ds_read_b128 v[120:123], v164 offset:16384
	ds_read_b128 v[124:127], v164 offset:24576
	s_waitcnt lgkmcnt(7)
	v_mfma_f32_16x16x32_bf16 v[64:67], v[96:99], v[0:3], 0
	v_mfma_f32_16x16x32_bf16 v[68:71], v[96:99], v[32:35], 0
	v_xor_b32_e32 v164, 0x80, v163
	ds_read_b128 v[96:99], v164
	s_waitcnt lgkmcnt(7)
	v_mfma_f32_16x16x32_bf16 v[72:75], v[100:103], v[0:3], 0
	v_mfma_f32_16x16x32_bf16 v[76:79], v[100:103], v[32:35], 0
	ds_read_b128 v[100:103], v164 offset:8192
	s_waitcnt lgkmcnt(7)
	v_mfma_f32_16x16x32_bf16 v[80:83], v[104:107], v[0:3], 0
	v_mfma_f32_16x16x32_bf16 v[84:87], v[104:107], v[32:35], 0
	ds_read_b128 v[104:107], v164 offset:16384
	s_waitcnt lgkmcnt(7)
	v_mfma_f32_16x16x32_bf16 v[88:91], v[108:111], v[0:3], 0
	v_mfma_f32_16x16x32_bf16 v[92:95], v[108:111], v[32:35], 0
	ds_read_b128 v[108:111], v164 offset:24576
	s_waitcnt lgkmcnt(7)
	v_mfma_f32_16x16x32_bf16 v[64:67], v[112:115], v[4:7], v[64:67]
	v_mfma_f32_16x16x32_bf16 v[68:71], v[112:115], v[36:39], v[68:71]
	v_xor_b32_e32 v164, 0xc0, v163
	ds_read_b128 v[112:115], v164
	s_waitcnt lgkmcnt(7)
	v_mfma_f32_16x16x32_bf16 v[72:75], v[116:119], v[4:7], v[72:75]
	v_mfma_f32_16x16x32_bf16 v[76:79], v[116:119], v[36:39], v[76:79]
	ds_read_b128 v[116:119], v164 offset:8192
	s_waitcnt lgkmcnt(7)
	v_mfma_f32_16x16x32_bf16 v[80:83], v[120:123], v[4:7], v[80:83]
	v_mfma_f32_16x16x32_bf16 v[84:87], v[120:123], v[36:39], v[84:87]
	ds_read_b128 v[120:123], v164 offset:16384
	s_waitcnt lgkmcnt(7)
	v_mfma_f32_16x16x32_bf16 v[88:91], v[124:127], v[4:7], v[88:91]
	v_mfma_f32_16x16x32_bf16 v[92:95], v[124:127], v[36:39], v[92:95]
	ds_read_b128 v[124:127], v164 offset:24576
	s_waitcnt lgkmcnt(7)
	v_mfma_f32_16x16x32_bf16 v[64:67], v[96:99], v[8:11], v[64:67]
	v_mfma_f32_16x16x32_bf16 v[68:71], v[96:99], v[40:43], v[68:71]
	v_xor_b32_e32 v164, 0x100, v163
	ds_read_b128 v[96:99], v164
	s_waitcnt lgkmcnt(7)
	v_mfma_f32_16x16x32_bf16 v[72:75], v[100:103], v[8:11], v[72:75]
	v_mfma_f32_16x16x32_bf16 v[76:79], v[100:103], v[40:43], v[76:79]
	ds_read_b128 v[100:103], v164 offset:8192
	s_waitcnt lgkmcnt(7)
	v_mfma_f32_16x16x32_bf16 v[80:83], v[104:107], v[8:11], v[80:83]
	v_mfma_f32_16x16x32_bf16 v[84:87], v[104:107], v[40:43], v[84:87]
	ds_read_b128 v[104:107], v164 offset:16384
	s_waitcnt lgkmcnt(7)
	v_mfma_f32_16x16x32_bf16 v[88:91], v[108:111], v[8:11], v[88:91]
	v_mfma_f32_16x16x32_bf16 v[92:95], v[108:111], v[40:43], v[92:95]
	ds_read_b128 v[108:111], v164 offset:24576
	s_waitcnt lgkmcnt(7)
	v_mfma_f32_16x16x32_bf16 v[64:67], v[112:115], v[12:15], v[64:67]
	v_mfma_f32_16x16x32_bf16 v[68:71], v[112:115], v[44:47], v[68:71]
	v_xor_b32_e32 v164, 0x140, v163
	ds_read_b128 v[112:115], v164
	s_waitcnt lgkmcnt(7)
	v_mfma_f32_16x16x32_bf16 v[72:75], v[116:119], v[12:15], v[72:75]
	v_mfma_f32_16x16x32_bf16 v[76:79], v[116:119], v[44:47], v[76:79]
	ds_read_b128 v[116:119], v164 offset:8192
	s_waitcnt lgkmcnt(7)
	v_mfma_f32_16x16x32_bf16 v[80:83], v[120:123], v[12:15], v[80:83]
	v_mfma_f32_16x16x32_bf16 v[84:87], v[120:123], v[44:47], v[84:87]
	ds_read_b128 v[120:123], v164 offset:16384
	s_waitcnt lgkmcnt(7)
	v_mfma_f32_16x16x32_bf16 v[88:91], v[124:127], v[12:15], v[88:91]
	v_mfma_f32_16x16x32_bf16 v[92:95], v[124:127], v[44:47], v[92:95]
	ds_read_b128 v[124:127], v164 offset:24576
	s_waitcnt lgkmcnt(7)
	v_mfma_f32_16x16x32_bf16 v[64:67], v[96:99], v[16:19], v[64:67]
	v_mfma_f32_16x16x32_bf16 v[68:71], v[96:99], v[48:51], v[68:71]
	v_xor_b32_e32 v164, 0x180, v163
	ds_read_b128 v[96:99], v164
	s_waitcnt lgkmcnt(7)
	v_mfma_f32_16x16x32_bf16 v[72:75], v[100:103], v[16:19], v[72:75]
	v_mfma_f32_16x16x32_bf16 v[76:79], v[100:103], v[48:51], v[76:79]
	ds_read_b128 v[100:103], v164 offset:8192
	s_waitcnt lgkmcnt(7)
	v_mfma_f32_16x16x32_bf16 v[80:83], v[104:107], v[16:19], v[80:83]
	v_mfma_f32_16x16x32_bf16 v[84:87], v[104:107], v[48:51], v[84:87]
	ds_read_b128 v[104:107], v164 offset:16384
	s_waitcnt lgkmcnt(7)
	v_mfma_f32_16x16x32_bf16 v[88:91], v[108:111], v[16:19], v[88:91]
	v_mfma_f32_16x16x32_bf16 v[92:95], v[108:111], v[48:51], v[92:95]
	ds_read_b128 v[108:111], v164 offset:24576
	s_waitcnt lgkmcnt(7)
	v_mfma_f32_16x16x32_bf16 v[64:67], v[112:115], v[20:23], v[64:67]
	v_mfma_f32_16x16x32_bf16 v[68:71], v[112:115], v[52:55], v[68:71]
	v_xor_b32_e32 v164, 0x1c0, v163
	ds_read_b128 v[112:115], v164
	s_waitcnt lgkmcnt(7)
	v_mfma_f32_16x16x32_bf16 v[72:75], v[116:119], v[20:23], v[72:75]
	v_mfma_f32_16x16x32_bf16 v[76:79], v[116:119], v[52:55], v[76:79]
	ds_read_b128 v[116:119], v164 offset:8192
	s_waitcnt lgkmcnt(7)
	v_mfma_f32_16x16x32_bf16 v[80:83], v[120:123], v[20:23], v[80:83]
	v_mfma_f32_16x16x32_bf16 v[84:87], v[120:123], v[52:55], v[84:87]
	ds_read_b128 v[120:123], v164 offset:16384
	s_waitcnt lgkmcnt(7)
	v_mfma_f32_16x16x32_bf16 v[88:91], v[124:127], v[20:23], v[88:91]
	v_mfma_f32_16x16x32_bf16 v[92:95], v[124:127], v[52:55], v[92:95]
	ds_read_b128 v[124:127], v164 offset:24576
	s_waitcnt lgkmcnt(7)
	v_mfma_f32_16x16x32_bf16 v[64:67], v[96:99], v[24:27], v[64:67]
	v_mfma_f32_16x16x32_bf16 v[68:71], v[96:99], v[56:59], v[68:71]
	s_waitcnt lgkmcnt(6)
	v_mfma_f32_16x16x32_bf16 v[72:75], v[100:103], v[24:27], v[72:75]
	v_mfma_f32_16x16x32_bf16 v[76:79], v[100:103], v[56:59], v[76:79]
	s_waitcnt lgkmcnt(5)
	v_mfma_f32_16x16x32_bf16 v[80:83], v[104:107], v[24:27], v[80:83]
	v_mfma_f32_16x16x32_bf16 v[84:87], v[104:107], v[56:59], v[84:87]
	s_waitcnt lgkmcnt(4)
	v_mfma_f32_16x16x32_bf16 v[88:91], v[108:111], v[24:27], v[88:91]
	v_mfma_f32_16x16x32_bf16 v[92:95], v[108:111], v[56:59], v[92:95]
	s_waitcnt lgkmcnt(3)
	v_mfma_f32_16x16x32_bf16 v[64:67], v[112:115], v[28:31], v[64:67]
	v_mfma_f32_16x16x32_bf16 v[68:71], v[112:115], v[60:63], v[68:71]
	s_waitcnt lgkmcnt(2)
	v_mfma_f32_16x16x32_bf16 v[72:75], v[116:119], v[28:31], v[72:75]
	v_mfma_f32_16x16x32_bf16 v[76:79], v[116:119], v[60:63], v[76:79]
	s_waitcnt lgkmcnt(1)
	v_mfma_f32_16x16x32_bf16 v[80:83], v[120:123], v[28:31], v[80:83]
	v_mfma_f32_16x16x32_bf16 v[84:87], v[120:123], v[60:63], v[84:87]
	s_waitcnt lgkmcnt(0)
	v_mfma_f32_16x16x32_bf16 v[88:91], v[124:127], v[28:31], v[88:91]
	v_mfma_f32_16x16x32_bf16 v[92:95], v[124:127], v[60:63], v[92:95]
	v_mov_b32_e32 v169, v165
	v_mov_b32_e32 v170, v166
	v_mov_b32_e32 v171, v167
	v_mov_b32_e32 v172, v168
	ds_read_u16 v144, v169
	ds_read_u16 v145, v170
	ds_read_u16 v146, v171
	ds_read_u16 v147, v172
	ds_read_u16 v148, v169 offset:8192
	ds_read_u16 v149, v170 offset:8192
	ds_read_u16 v150, v171 offset:8192
	ds_read_u16 v151, v172 offset:8192
	ds_read_u16 v152, v169 offset:16384
	ds_read_u16 v153, v170 offset:16384
	ds_read_u16 v154, v171 offset:16384
	ds_read_u16 v155, v172 offset:16384
	ds_read_u16 v156, v169 offset:24576
	ds_read_u16 v157, v170 offset:24576
	ds_read_u16 v158, v171 offset:24576
	ds_read_u16 v159, v172 offset:24576
	s_nop 7
	v_fma_f32 v178, v64, s53, v173
	v_fma_f32 v179, v65, s53, v173
	v_fma_f32 v180, v66, s53, v173
	v_fma_f32 v181, v67, s53, v173
	v_fma_f32 v182, v72, s53, v173
	v_fma_f32 v183, v73, s53, v173
	v_fma_f32 v184, v74, s53, v173
	v_fma_f32 v185, v75, s53, v173
	v_fma_f32 v186, v68, s53, v174
	v_fma_f32 v187, v69, s53, v174
	v_fma_f32 v188, v70, s53, v174
	v_fma_f32 v189, v71, s53, v174
	v_fma_f32 v190, v76, s53, v174
	v_fma_f32 v191, v77, s53, v174
	v_fma_f32 v192, v78, s53, v174
	v_fma_f32 v193, v79, s53, v174
	v_exp_f32_e32 v178, v178
	v_exp_f32_e32 v179, v179
	v_exp_f32_e32 v180, v180
	v_exp_f32_e32 v181, v181
	v_exp_f32_e32 v182, v182
	v_exp_f32_e32 v183, v183
	v_exp_f32_e32 v184, v184
	v_exp_f32_e32 v185, v185
	v_exp_f32_e32 v186, v186
	v_exp_f32_e32 v187, v187
	v_exp_f32_e32 v188, v188
	v_exp_f32_e32 v189, v189
	v_exp_f32_e32 v190, v190
	v_exp_f32_e32 v191, v191
	v_exp_f32_e32 v192, v192
	v_exp_f32_e32 v193, v193
	v_add_f32_e32 v178, 1.0, v178
	v_add_f32_e32 v179, 1.0, v179
	v_add_f32_e32 v180, 1.0, v180
	v_add_f32_e32 v181, 1.0, v181
	v_add_f32_e32 v182, 1.0, v182
	v_add_f32_e32 v183, 1.0, v183
	v_add_f32_e32 v184, 1.0, v184
	v_add_f32_e32 v185, 1.0, v185
	v_add_f32_e32 v186, 1.0, v186
	v_add_f32_e32 v187, 1.0, v187
	v_add_f32_e32 v188, 1.0, v188
	v_add_f32_e32 v189, 1.0, v189
	v_add_f32_e32 v190, 1.0, v190
	v_add_f32_e32 v191, 1.0, v191
	v_add_f32_e32 v192, 1.0, v192
	v_add_f32_e32 v193, 1.0, v193
	v_rcp_f32_e32 v178, v178
	v_rcp_f32_e32 v179, v179
	v_rcp_f32_e32 v180, v180
	v_rcp_f32_e32 v181, v181
	v_rcp_f32_e32 v182, v182
	v_rcp_f32_e32 v183, v183
	v_rcp_f32_e32 v184, v184
	v_rcp_f32_e32 v185, v185
	v_rcp_f32_e32 v186, v186
	v_rcp_f32_e32 v187, v187
	v_rcp_f32_e32 v188, v188
	v_rcp_f32_e32 v189, v189
	v_rcp_f32_e32 v190, v190
	v_rcp_f32_e32 v191, v191
	v_rcp_f32_e32 v192, v192
	v_rcp_f32_e32 v193, v193
	v_mul_f32_e32 v178, v175, v178
	v_mul_f32_e32 v179, v175, v179
	v_mul_f32_e32 v180, v175, v180
	v_mul_f32_e32 v181, v175, v181
	v_mul_f32_e32 v182, v175, v182
	v_mul_f32_e32 v183, v175, v183
	v_mul_f32_e32 v184, v175, v184
	v_mul_f32_e32 v185, v175, v185
	v_exp_f32_e32 v96, v178
	v_exp_f32_e32 v97, v179
	v_exp_f32_e32 v98, v180
	v_exp_f32_e32 v99, v181
	v_exp_f32_e32 v100, v182
	v_exp_f32_e32 v101, v183
	v_exp_f32_e32 v102, v184
	v_exp_f32_e32 v103, v185
	s_nop 0
	v_fma_f32 v194, -v96, v96, 1.0
	v_fma_f32 v195, -v97, v97, 1.0
	v_fma_f32 v196, -v98, v98, 1.0
	v_fma_f32 v197, -v99, v99, 1.0
	v_fma_f32 v198, -v100, v100, 1.0
	v_fma_f32 v199, -v101, v101, 1.0
	v_fma_f32 v200, -v102, v102, 1.0
	v_fma_f32 v201, -v103, v103, 1.0
	v_max_f32_e32 v194, 0, v194
	v_max_f32_e32 v195, 0, v195
	v_max_f32_e32 v196, 0, v196
	v_max_f32_e32 v197, 0, v197
	v_max_f32_e32 v198, 0, v198
	v_max_f32_e32 v199, 0, v199
	v_max_f32_e32 v200, 0, v200
	v_max_f32_e32 v201, 0, v201
	v_sqrt_f32_e32 v194, v194
	v_sqrt_f32_e32 v195, v195
	v_sqrt_f32_e32 v196, v196
	v_sqrt_f32_e32 v197, v197
	v_sqrt_f32_e32 v198, v198
	v_sqrt_f32_e32 v199, v199
	v_sqrt_f32_e32 v200, v200
	v_sqrt_f32_e32 v201, v201
	s_waitcnt lgkmcnt(8)
	v_lshlrev_b32_e32 v144, 16, v144
	v_lshlrev_b32_e32 v145, 16, v145
	v_lshlrev_b32_e32 v146, 16, v146
	v_lshlrev_b32_e32 v147, 16, v147
	v_lshlrev_b32_e32 v148, 16, v148
	v_lshlrev_b32_e32 v149, 16, v149
	v_lshlrev_b32_e32 v150, 16, v150
	v_lshlrev_b32_e32 v151, 16, v151
	v_mul_f32_e32 v194, v194, v186
	v_mul_f32_e32 v195, v195, v187
	v_mul_f32_e32 v196, v196, v188
	v_mul_f32_e32 v197, v197, v189
	v_mul_f32_e32 v198, v198, v190
	v_mul_f32_e32 v199, v199, v191
	v_mul_f32_e32 v200, v200, v192
	v_mul_f32_e32 v201, v201, v193
	v_mul_f32_e32 v144, v194, v144
	v_mul_f32_e32 v145, v195, v145
	v_mul_f32_e32 v146, v196, v146
	v_mul_f32_e32 v147, v197, v147
	v_mul_f32_e32 v148, v198, v148
	v_mul_f32_e32 v149, v199, v149
	v_mul_f32_e32 v150, v200, v150
	v_mul_f32_e32 v151, v201, v151
	v_fma_f32 v178, v80, s53, v173
	v_fma_f32 v179, v81, s53, v173
	v_fma_f32 v180, v82, s53, v173
	v_fma_f32 v181, v83, s53, v173
	v_fma_f32 v182, v88, s53, v173
	v_fma_f32 v183, v89, s53, v173
	v_fma_f32 v184, v90, s53, v173
	v_fma_f32 v185, v91, s53, v173
	v_fma_f32 v186, v84, s53, v174
	v_fma_f32 v187, v85, s53, v174
	v_fma_f32 v188, v86, s53, v174
	v_fma_f32 v189, v87, s53, v174
	v_fma_f32 v190, v92, s53, v174
	v_fma_f32 v191, v93, s53, v174
	v_fma_f32 v192, v94, s53, v174
	v_fma_f32 v193, v95, s53, v174
	v_exp_f32_e32 v178, v178
	v_exp_f32_e32 v179, v179
	v_exp_f32_e32 v180, v180
	v_exp_f32_e32 v181, v181
	v_exp_f32_e32 v182, v182
	v_exp_f32_e32 v183, v183
	v_exp_f32_e32 v184, v184
	v_exp_f32_e32 v185, v185
	v_exp_f32_e32 v186, v186
	v_exp_f32_e32 v187, v187
	v_exp_f32_e32 v188, v188
	v_exp_f32_e32 v189, v189
	v_exp_f32_e32 v190, v190
	v_exp_f32_e32 v191, v191
	v_exp_f32_e32 v192, v192
	v_exp_f32_e32 v193, v193
	v_add_f32_e32 v178, 1.0, v178
	v_add_f32_e32 v179, 1.0, v179
	v_add_f32_e32 v180, 1.0, v180
	v_add_f32_e32 v181, 1.0, v181
	v_add_f32_e32 v182, 1.0, v182
	v_add_f32_e32 v183, 1.0, v183
	v_add_f32_e32 v184, 1.0, v184
	v_add_f32_e32 v185, 1.0, v185
	v_add_f32_e32 v186, 1.0, v186
	v_add_f32_e32 v187, 1.0, v187
	v_add_f32_e32 v188, 1.0, v188
	v_add_f32_e32 v189, 1.0, v189
	v_add_f32_e32 v190, 1.0, v190
	v_add_f32_e32 v191, 1.0, v191
	v_add_f32_e32 v192, 1.0, v192
	v_add_f32_e32 v193, 1.0, v193
	v_rcp_f32_e32 v178, v178
	v_rcp_f32_e32 v179, v179
	v_rcp_f32_e32 v180, v180
	v_rcp_f32_e32 v181, v181
	v_rcp_f32_e32 v182, v182
	v_rcp_f32_e32 v183, v183
	v_rcp_f32_e32 v184, v184
	v_rcp_f32_e32 v185, v185
	v_rcp_f32_e32 v186, v186
	v_rcp_f32_e32 v187, v187
	v_rcp_f32_e32 v188, v188
	v_rcp_f32_e32 v189, v189
	v_rcp_f32_e32 v190, v190
	v_rcp_f32_e32 v191, v191
	v_rcp_f32_e32 v192, v192
	v_rcp_f32_e32 v193, v193
	v_mul_f32_e32 v178, v175, v178
	v_mul_f32_e32 v179, v175, v179
	v_mul_f32_e32 v180, v175, v180
	v_mul_f32_e32 v181, v175, v181
	v_mul_f32_e32 v182, v175, v182
	v_mul_f32_e32 v183, v175, v183
	v_mul_f32_e32 v184, v175, v184
	v_mul_f32_e32 v185, v175, v185
	v_exp_f32_e32 v104, v178
	v_exp_f32_e32 v105, v179
	v_exp_f32_e32 v106, v180
	v_exp_f32_e32 v107, v181
	v_exp_f32_e32 v108, v182
	v_exp_f32_e32 v109, v183
	v_exp_f32_e32 v110, v184
	v_exp_f32_e32 v111, v185
	s_nop 0
	v_fma_f32 v194, -v104, v104, 1.0
	v_fma_f32 v195, -v105, v105, 1.0
	v_fma_f32 v196, -v106, v106, 1.0
	v_fma_f32 v197, -v107, v107, 1.0
	v_fma_f32 v198, -v108, v108, 1.0
	v_fma_f32 v199, -v109, v109, 1.0
	v_fma_f32 v200, -v110, v110, 1.0
	v_fma_f32 v201, -v111, v111, 1.0
	v_max_f32_e32 v194, 0, v194
	v_max_f32_e32 v195, 0, v195
	v_max_f32_e32 v196, 0, v196
	v_max_f32_e32 v197, 0, v197
	v_max_f32_e32 v198, 0, v198
	v_max_f32_e32 v199, 0, v199
	v_max_f32_e32 v200, 0, v200
	v_max_f32_e32 v201, 0, v201
	v_sqrt_f32_e32 v194, v194
	v_sqrt_f32_e32 v195, v195
	v_sqrt_f32_e32 v196, v196
	v_sqrt_f32_e32 v197, v197
	v_sqrt_f32_e32 v198, v198
	v_sqrt_f32_e32 v199, v199
	v_sqrt_f32_e32 v200, v200
	v_sqrt_f32_e32 v201, v201
	s_waitcnt lgkmcnt(0)
	v_lshlrev_b32_e32 v152, 16, v152
	v_lshlrev_b32_e32 v153, 16, v153
	v_lshlrev_b32_e32 v154, 16, v154
	v_lshlrev_b32_e32 v155, 16, v155
	v_lshlrev_b32_e32 v156, 16, v156
	v_lshlrev_b32_e32 v157, 16, v157
	v_lshlrev_b32_e32 v158, 16, v158
	v_lshlrev_b32_e32 v159, 16, v159
	v_mul_f32_e32 v194, v194, v186
	v_mul_f32_e32 v195, v195, v187
	v_mul_f32_e32 v196, v196, v188
	v_mul_f32_e32 v197, v197, v189
	v_mul_f32_e32 v198, v198, v190
	v_mul_f32_e32 v199, v199, v191
	v_mul_f32_e32 v200, v200, v192
	v_mul_f32_e32 v201, v201, v193
	v_mul_f32_e32 v152, v194, v152
	v_mul_f32_e32 v153, v195, v153
	v_mul_f32_e32 v154, v196, v154
	v_mul_f32_e32 v155, v197, v155
	v_mul_f32_e32 v156, v198, v156
	v_mul_f32_e32 v157, v199, v157
	v_mul_f32_e32 v158, v200, v158
	v_mul_f32_e32 v159, v201, v159
	v_fma_f32 v146, v98, v147, v146
	v_fma_f32 v150, v102, v151, v150
	v_fma_f32 v154, v106, v155, v154
	v_fma_f32 v158, v110, v159, v158
	v_mul_f32_e32 v98, v98, v99
	v_mul_f32_e32 v102, v102, v103
	v_mul_f32_e32 v106, v106, v107
	v_mul_f32_e32 v110, v110, v111
	v_fma_f32 v145, v97, v146, v145
	v_fma_f32 v149, v101, v150, v149
	v_fma_f32 v153, v105, v154, v153
	v_fma_f32 v157, v109, v158, v157
	v_mul_f32_e32 v97, v97, v98
	v_mul_f32_e32 v101, v101, v102
	v_mul_f32_e32 v105, v105, v106
	v_mul_f32_e32 v109, v109, v110
	v_fma_f32 v144, v96, v145, v144
	v_fma_f32 v148, v100, v149, v148
	v_fma_f32 v152, v104, v153, v152
	v_fma_f32 v156, v108, v157, v156
	v_mul_f32_e32 v96, v96, v97
	v_mul_f32_e32 v100, v100, v101
	v_mul_f32_e32 v104, v104, v105
	v_mul_f32_e32 v108, v108, v109
	ds_bpermute_b32 v178, v204, v96
	ds_bpermute_b32 v182, v204, v144
	ds_bpermute_b32 v179, v204, v100
	ds_bpermute_b32 v183, v204, v148
	ds_bpermute_b32 v180, v204, v104
	ds_bpermute_b32 v184, v204, v152
	ds_bpermute_b32 v181, v204, v108
	ds_bpermute_b32 v185, v204, v156
	s_waitcnt lgkmcnt(0)
	v_fma_f32 v186, v182, v96, v144
	v_cndmask_b32_e64 v178, 1.0, v178, s[34:35]
	v_fma_f32 v187, v183, v100, v148
	v_cndmask_b32_e64 v179, 1.0, v179, s[34:35]
	v_fma_f32 v188, v184, v104, v152
	v_cndmask_b32_e64 v180, 1.0, v180, s[34:35]
	v_fma_f32 v189, v185, v108, v156
	v_cndmask_b32_e64 v181, 1.0, v181, s[34:35]
	v_cndmask_b32_e64 v223, v144, v186, s[34:35]
	v_mul_f32_e32 v219, v96, v178
	v_cndmask_b32_e64 v224, v148, v187, s[34:35]
	v_mul_f32_e32 v220, v100, v179
	v_cndmask_b32_e64 v225, v152, v188, s[34:35]
	v_mul_f32_e32 v221, v104, v180
	v_cndmask_b32_e64 v226, v156, v189, s[34:35]
	v_mul_f32_e32 v222, v108, v181
	ds_bpermute_b32 v178, v205, v219
	ds_bpermute_b32 v182, v205, v223
	ds_bpermute_b32 v179, v205, v220
	ds_bpermute_b32 v183, v205, v224
	ds_bpermute_b32 v180, v205, v221
	ds_bpermute_b32 v184, v205, v225
	ds_bpermute_b32 v181, v205, v222
	ds_bpermute_b32 v185, v205, v226
	s_waitcnt lgkmcnt(0)
	v_fma_f32 v186, v182, v219, v223
	v_cndmask_b32_e64 v178, 1.0, v178, s[36:37]
	v_fma_f32 v187, v183, v220, v224
	v_cndmask_b32_e64 v179, 1.0, v179, s[36:37]
	v_fma_f32 v188, v184, v221, v225
	v_cndmask_b32_e64 v180, 1.0, v180, s[36:37]
	v_fma_f32 v189, v185, v222, v226
	v_cndmask_b32_e64 v181, 1.0, v181, s[36:37]
	v_cndmask_b32_e64 v223, v223, v186, s[36:37]
	v_mul_f32_e32 v219, v219, v178
	v_cndmask_b32_e64 v224, v224, v187, s[36:37]
	v_mul_f32_e32 v220, v220, v179
	v_cndmask_b32_e64 v225, v225, v188, s[36:37]
	v_mul_f32_e32 v221, v221, v180
	v_cndmask_b32_e64 v226, v226, v189, s[36:37]
	v_mul_f32_e32 v222, v222, v181
	ds_bpermute_b32 v227, v204, v219
	ds_bpermute_b32 v231, v204, v223
	ds_bpermute_b32 v235, v206, v219
	ds_bpermute_b32 v239, v206, v223
	ds_bpermute_b32 v228, v204, v220
	ds_bpermute_b32 v232, v204, v224
	ds_bpermute_b32 v236, v206, v220
	ds_bpermute_b32 v244, v206, v224
	ds_bpermute_b32 v229, v204, v221
	ds_bpermute_b32 v233, v204, v225
	ds_bpermute_b32 v237, v206, v221
	ds_bpermute_b32 v245, v206, v225
	ds_bpermute_b32 v230, v204, v222
	ds_bpermute_b32 v234, v204, v226
	ds_bpermute_b32 v238, v206, v222
	ds_bpermute_b32 v246, v206, v226
	s_waitcnt lgkmcnt(0)
	v_cndmask_b32_e64 v227, 1.0, v227, s[34:35]
	v_cndmask_b32_e64 v231, 0, v231, s[34:35]
	v_cndmask_b32_e64 v228, 1.0, v228, s[34:35]
	v_cndmask_b32_e64 v232, 0, v232, s[34:35]
	v_cndmask_b32_e64 v229, 1.0, v229, s[34:35]
	v_cndmask_b32_e64 v233, 0, v233, s[34:35]
	v_cndmask_b32_e64 v230, 1.0, v230, s[34:35]
	v_cndmask_b32_e64 v234, 0, v234, s[34:35]
	v_mov_b32_e32 v190, v238
	v_mov_b32_e32 v194, v246
	v_mov_b32_e32 v198, v190
	v_mov_b32_e32 v201, v194
	v_fma_f32 v194, v194, v237, v245
	v_mul_f32_e32 v190, v190, v237
	v_mov_b32_e32 v199, v190
	v_mov_b32_e32 v177, v194
	v_fma_f32 v194, v194, v236, v244
	v_mul_f32_e32 v190, v190, v236
	v_mov_b32_e32 v200, v190
	v_mov_b32_e32 v203, v194
	v_fma_f32 v194, v194, v235, v239
	v_mul_f32_e32 v190, v190, v235
	v_mov_b32_e32 v191, v194
	ds_write_b64 v207, v[190:191]
	s_cmp_eq_u32 s13, 17
	s_cbranch_scc1 .Lmylru_g0_8
	s_waitcnt vmcnt(8)
	s_branch .Lmylru_g1_8

.Lmylru_g1_8:
	s_waitcnt lgkmcnt(0)
	s_barrier
	ds_read_b64 v[178:179], v208 offset:512
	ds_read_b64 v[180:181], v208
	s_waitcnt lgkmcnt(0)
	v_fma_f32 v182, v176, v178, v179
	v_cndmask_b32_e64 v183, v176, v182, s[38:39]
	v_fma_f32 v176, v182, v180, v181
	v_fma_f32 v184, v183, v200, v203
	v_fma_f32 v185, v183, v199, v177
	v_fma_f32 v186, v183, v198, v201
	v_mov_b32_e32 v187, v183
	v_fma_f32 v184, v184, v227, v231
	v_fma_f32 v185, v185, v228, v232
	v_fma_f32 v186, v186, v229, v233
	v_fma_f32 v187, v187, v230, v234
	v_fma_f32 v144, v184, v96, v144
	v_fma_f32 v148, v185, v100, v148
	v_fma_f32 v152, v186, v104, v152
	v_fma_f32 v156, v187, v108, v156
	v_fma_f32 v145, v184, v97, v145
	v_fma_f32 v149, v185, v101, v149
	v_fma_f32 v153, v186, v105, v153
	v_fma_f32 v157, v187, v109, v157
	v_fma_f32 v146, v184, v98, v146
	v_fma_f32 v150, v185, v102, v150
	v_fma_f32 v154, v186, v106, v154
	v_fma_f32 v158, v187, v110, v158
	v_fma_f32 v147, v184, v99, v147
	v_fma_f32 v151, v185, v103, v151
	v_fma_f32 v155, v186, v107, v155
	v_fma_f32 v159, v187, v111, v159
	s_cmp_eq_u32 s13, 17
	s_cbranch_scc1 .Lmylru_w0_7
	s_waitcnt vmcnt(8)
	s_branch .Lmylru_w1_7

.Lmylru_w1_7:
	v_lshrrev_b32_e32 v184, 11, v210
	v_and_b32_e32 v185, 0x7ff, v210
	v_lshl_add_u32 v184, v184, 7, v185
	v_add_u32_e32 v184, 0x20800, v184
	ds_read_u16 v128, v184
	ds_read_u16 v129, v184 offset:128
	ds_read_u16 v130, v184 offset:256
	ds_read_u16 v131, v184 offset:384
	ds_read_u16 v132, v184 offset:2048
	ds_read_u16 v133, v184 offset:2176
	ds_read_u16 v134, v184 offset:2304
	ds_read_u16 v135, v184 offset:2432
	ds_read_u16 v136, v184 offset:4096
	ds_read_u16 v137, v184 offset:4224
	ds_read_u16 v138, v184 offset:4352
	ds_read_u16 v139, v184 offset:4480
	ds_read_u16 v140, v184 offset:6144
	ds_read_u16 v141, v184 offset:6272
	ds_read_u16 v142, v184 offset:6400
	ds_read_u16 v143, v184 offset:6528
	s_waitcnt lgkmcnt(0)
	v_lshlrev_b32_e32 v178, 16, v247
	v_add_f32_e32 v144, v144, v178
	v_lshlrev_b32_e32 v128, 16, v128
	v_mul_f32_e32 v144, v144, v128
	v_cvt_pk_bf16_f32 v144, v144, v144
	v_and_b32_e32 v179, 0xffff0000, v247
	v_add_f32_e32 v145, v145, v179
	v_lshlrev_b32_e32 v129, 16, v129
	v_mul_f32_e32 v145, v145, v129
	v_cvt_pk_bf16_f32 v145, v145, v145
	v_lshlrev_b32_e32 v180, 16, v248
	v_add_f32_e32 v146, v146, v180
	v_lshlrev_b32_e32 v130, 16, v130
	v_mul_f32_e32 v146, v146, v130
	v_cvt_pk_bf16_f32 v146, v146, v146
	v_and_b32_e32 v181, 0xffff0000, v248
	v_add_f32_e32 v147, v147, v181
	v_lshlrev_b32_e32 v131, 16, v131
	v_mul_f32_e32 v147, v147, v131
	v_cvt_pk_bf16_f32 v147, v147, v147
	v_lshlrev_b32_e32 v178, 16, v249
	v_add_f32_e32 v148, v148, v178
	v_lshlrev_b32_e32 v132, 16, v132
	v_mul_f32_e32 v148, v148, v132
	v_cvt_pk_bf16_f32 v148, v148, v148
	v_and_b32_e32 v179, 0xffff0000, v249
	v_add_f32_e32 v149, v149, v179
	v_lshlrev_b32_e32 v133, 16, v133
	v_mul_f32_e32 v149, v149, v133
	v_cvt_pk_bf16_f32 v149, v149, v149
	v_lshlrev_b32_e32 v180, 16, v250
	v_add_f32_e32 v150, v150, v180
	v_lshlrev_b32_e32 v134, 16, v134
	v_mul_f32_e32 v150, v150, v134
	v_cvt_pk_bf16_f32 v150, v150, v150
	v_and_b32_e32 v181, 0xffff0000, v250
	v_add_f32_e32 v151, v151, v181
	v_lshlrev_b32_e32 v135, 16, v135
	v_mul_f32_e32 v151, v151, v135
	v_cvt_pk_bf16_f32 v151, v151, v151
	v_lshlrev_b32_e32 v178, 16, v251
	v_add_f32_e32 v152, v152, v178
	v_lshlrev_b32_e32 v136, 16, v136
	v_mul_f32_e32 v152, v152, v136
	v_cvt_pk_bf16_f32 v152, v152, v152
	v_and_b32_e32 v179, 0xffff0000, v251
	v_add_f32_e32 v153, v153, v179
	v_lshlrev_b32_e32 v137, 16, v137
	v_mul_f32_e32 v153, v153, v137
	v_cvt_pk_bf16_f32 v153, v153, v153
	v_lshlrev_b32_e32 v180, 16, v252
	v_add_f32_e32 v154, v154, v180
	v_lshlrev_b32_e32 v138, 16, v138
	v_mul_f32_e32 v154, v154, v138
	v_cvt_pk_bf16_f32 v154, v154, v154
	v_and_b32_e32 v181, 0xffff0000, v252
	v_add_f32_e32 v155, v155, v181
	v_lshlrev_b32_e32 v139, 16, v139
	v_mul_f32_e32 v155, v155, v139
	v_cvt_pk_bf16_f32 v155, v155, v155
	v_lshlrev_b32_e32 v178, 16, v253
	v_add_f32_e32 v156, v156, v178
	v_lshlrev_b32_e32 v140, 16, v140
	v_mul_f32_e32 v156, v156, v140
	v_cvt_pk_bf16_f32 v156, v156, v156
	v_and_b32_e32 v179, 0xffff0000, v253
	v_add_f32_e32 v157, v157, v179
	v_lshlrev_b32_e32 v141, 16, v141
	v_mul_f32_e32 v157, v157, v141
	v_cvt_pk_bf16_f32 v157, v157, v157
	v_lshlrev_b32_e32 v180, 16, v254
	v_add_f32_e32 v158, v158, v180
	v_lshlrev_b32_e32 v142, 16, v142
	v_mul_f32_e32 v158, v158, v142
	v_cvt_pk_bf16_f32 v158, v158, v158
	v_and_b32_e32 v181, 0xffff0000, v254
	v_add_f32_e32 v159, v159, v181
	v_lshlrev_b32_e32 v143, 16, v143
	v_mul_f32_e32 v159, v159, v143
	v_cvt_pk_bf16_f32 v159, v159, v159
	v_add_u32_e32 v182, 0x0, v210
	v_add_u32_e32 v183, 0x1000, v182
	global_store_short v182, v144, s[42:43]
	global_store_short v182, v145, s[42:43] offset:2048
	global_store_short v183, v146, s[42:43]
	global_store_short v183, v147, s[42:43] offset:2048
	v_add_u32_e32 v182, 0x8000, v210
	v_add_u32_e32 v183, 0x1000, v182
	global_store_short v182, v148, s[42:43]
	global_store_short v182, v149, s[42:43] offset:2048
	global_store_short v183, v150, s[42:43]
	global_store_short v183, v151, s[42:43] offset:2048
	v_add_u32_e32 v182, 0x10000, v210
	v_add_u32_e32 v183, 0x1000, v182
	global_store_short v182, v152, s[42:43]
	global_store_short v182, v153, s[42:43] offset:2048
	global_store_short v183, v154, s[42:43]
	global_store_short v183, v155, s[42:43] offset:2048
	v_add_u32_e32 v182, 0x18000, v210
	v_add_u32_e32 v183, 0x1000, v182
	global_store_short v182, v156, s[42:43]
	global_store_short v182, v157, s[42:43] offset:2048
	global_store_short v183, v158, s[42:43]
	global_store_short v183, v159, s[42:43] offset:2048
	s_add_i32 s13, s13, 1
	s_cmp_eq_u32 s13, 2
	s_cbranch_scc1 .Lmylru_t0_9
	s_waitcnt vmcnt(16)
	s_branch .Lmylru_t1_9

.Lmylru_t1_9:
	s_barrier
	s_sub_i32 s54, 17, s13
	s_lshl_b32 s55, s54, 14
	s_lshl_b32 s56, s6, 11
	s_add_i32 s55, s55, s56
	s_add_u32 s44, s22, s55
	s_addc_u32 s45, s23, 0
	s_cmp_lt_u32 s13, 2
	s_sub_i32 s50, 1, s13
	s_lshl_b32 s50, s50, 7
	s_lshl_b32 s51, s9, 8
	s_add_i32 s51, s51, 0x8000
	s_add_i32 s51, s51, s50
	s_sub_i32 s50, 17, s13
	s_lshl_b32 s50, s50, 7
	s_lshl_b32 s57, s9, 11
	s_add_i32 s57, s57, s50
	s_cmp_lt_u32 s13, 2
	s_cselect_b32 s57, s51, s57
	s_lshl_b32 s57, s57, 11
	s_add_u32 s40, s18, s57
	s_addc_u32 s41, s19, 0
	s_add_u32 s42, s20, s57
	s_addc_u32 s43, s21, 0
	global_load_dword v247, v209, s[44:45]
	global_load_dword v248, v209, s[44:45] offset:256
	global_load_dword v249, v209, s[44:45] offset:512
	global_load_dword v250, v209, s[44:45] offset:768
	global_load_dword v251, v209, s[44:45] offset:1024
	global_load_dword v252, v209, s[44:45] offset:1280
	global_load_dword v253, v209, s[44:45] offset:1536
	global_load_dword v254, v209, s[44:45] offset:1792
	s_lshl_b32 s52, s6, 11
	s_add_i32 s52, s52, 0x20800
	s_mov_b32 m0, s52
	v_add_u32_e32 v182, 0x4000, v255
	global_load_lds_dwordx4 v255, s[40:41]
	s_add_i32 s52, s52, 0x400
	s_mov_b32 m0, s52
	s_nop 0
	global_load_lds_dwordx4 v182, s[40:41]
	s_cmp_eq_u32 s13, 17
	s_cbranch_scc1 .Lmylru_nodma_9
	s_add_i32 s58, s13, 1
	s_cmp_lt_u32 s58, 2
	s_sub_i32 s50, 1, s58
	s_lshl_b32 s50, s50, 7
	s_lshl_b32 s51, s9, 8
	s_add_i32 s51, s51, 0x8000
	s_add_i32 s51, s51, s50
	s_sub_i32 s50, 17, s58
	s_lshl_b32 s50, s50, 7
	s_lshl_b32 s59, s9, 11
	s_add_i32 s59, s59, s50
	s_cmp_lt_u32 s58, 2
	s_cselect_b32 s59, s51, s59
	s_lshl_b32 s52, s59, 11
	s_add_u32 s46, s16, s52
	s_addc_u32 s47, s17, 0
	s_lshl_b32 s52, s6, 13
	s_mov_b32 m0, s52
	s_add_i32 s52, s52, 0x400
	global_load_lds_dwordx4 v211, s[46:47]
	s_mov_b32 m0, s52
	s_add_i32 s52, s52, 0x400
	global_load_lds_dwordx4 v212, s[46:47]
	s_mov_b32 m0, s52
	s_add_i32 s52, s52, 0x400
	global_load_lds_dwordx4 v213, s[46:47]
	s_mov_b32 m0, s52
	s_add_i32 s52, s52, 0x400
	global_load_lds_dwordx4 v214, s[46:47]
	s_mov_b32 m0, s52
	s_add_i32 s52, s52, 0x400
	global_load_lds_dwordx4 v215, s[46:47]
	s_mov_b32 m0, s52
	s_add_i32 s52, s52, 0x400
	global_load_lds_dwordx4 v216, s[46:47]
	s_mov_b32 m0, s52
	s_add_i32 s52, s52, 0x400
	global_load_lds_dwordx4 v217, s[46:47]
	s_mov_b32 m0, s52
	s_nop 0
	global_load_lds_dwordx4 v218, s[46:47]
.Lmylru_nodma_9:
	v_or_b32_e32 v163, 0x10000, v162
	ds_read_b128 v[96:99], v163
	ds_read_b128 v[100:103], v163 offset:8192
	ds_read_b128 v[104:107], v163 offset:16384
	ds_read_b128 v[108:111], v163 offset:24576
	v_xor_b32_e32 v164, 0x40, v163
	ds_read_b128 v[112:115], v164
	ds_read_b128 v[116:119], v164 offset:8192
	ds_read_b128 v[120:123], v164 offset:16384
	ds_read_b128 v[124:127], v164 offset:24576
	s_waitcnt lgkmcnt(7)
	v_mfma_f32_16x16x32_bf16 v[64:67], v[96:99], v[0:3], 0
	v_mfma_f32_16x16x32_bf16 v[68:71], v[96:99], v[32:35], 0
	v_xor_b32_e32 v164, 0x80, v163
	ds_read_b128 v[96:99], v164
	s_waitcnt lgkmcnt(7)
	v_mfma_f32_16x16x32_bf16 v[72:75], v[100:103], v[0:3], 0
	v_mfma_f32_16x16x32_bf16 v[76:79], v[100:103], v[32:35], 0
	ds_read_b128 v[100:103], v164 offset:8192
	s_waitcnt lgkmcnt(7)
	v_mfma_f32_16x16x32_bf16 v[80:83], v[104:107], v[0:3], 0
	v_mfma_f32_16x16x32_bf16 v[84:87], v[104:107], v[32:35], 0
	ds_read_b128 v[104:107], v164 offset:16384
	s_waitcnt lgkmcnt(7)
	v_mfma_f32_16x16x32_bf16 v[88:91], v[108:111], v[0:3], 0
	v_mfma_f32_16x16x32_bf16 v[92:95], v[108:111], v[32:35], 0
	ds_read_b128 v[108:111], v164 offset:24576
	s_waitcnt lgkmcnt(7)
	v_mfma_f32_16x16x32_bf16 v[64:67], v[112:115], v[4:7], v[64:67]
	v_mfma_f32_16x16x32_bf16 v[68:71], v[112:115], v[36:39], v[68:71]
	v_xor_b32_e32 v164, 0xc0, v163
	ds_read_b128 v[112:115], v164
	s_waitcnt lgkmcnt(7)
	v_mfma_f32_16x16x32_bf16 v[72:75], v[116:119], v[4:7], v[72:75]
	v_mfma_f32_16x16x32_bf16 v[76:79], v[116:119], v[36:39], v[76:79]
	ds_read_b128 v[116:119], v164 offset:8192
	s_waitcnt lgkmcnt(7)
	v_mfma_f32_16x16x32_bf16 v[80:83], v[120:123], v[4:7], v[80:83]
	v_mfma_f32_16x16x32_bf16 v[84:87], v[120:123], v[36:39], v[84:87]
	ds_read_b128 v[120:123], v164 offset:16384
	s_waitcnt lgkmcnt(7)
	v_mfma_f32_16x16x32_bf16 v[88:91], v[124:127], v[4:7], v[88:91]
	v_mfma_f32_16x16x32_bf16 v[92:95], v[124:127], v[36:39], v[92:95]
	ds_read_b128 v[124:127], v164 offset:24576
	s_waitcnt lgkmcnt(7)
	v_mfma_f32_16x16x32_bf16 v[64:67], v[96:99], v[8:11], v[64:67]
	v_mfma_f32_16x16x32_bf16 v[68:71], v[96:99], v[40:43], v[68:71]
	v_xor_b32_e32 v164, 0x100, v163
	ds_read_b128 v[96:99], v164
	s_waitcnt lgkmcnt(7)
	v_mfma_f32_16x16x32_bf16 v[72:75], v[100:103], v[8:11], v[72:75]
	v_mfma_f32_16x16x32_bf16 v[76:79], v[100:103], v[40:43], v[76:79]
	ds_read_b128 v[100:103], v164 offset:8192
	s_waitcnt lgkmcnt(7)
	v_mfma_f32_16x16x32_bf16 v[80:83], v[104:107], v[8:11], v[80:83]
	v_mfma_f32_16x16x32_bf16 v[84:87], v[104:107], v[40:43], v[84:87]
	ds_read_b128 v[104:107], v164 offset:16384
	s_waitcnt lgkmcnt(7)
	v_mfma_f32_16x16x32_bf16 v[88:91], v[108:111], v[8:11], v[88:91]
	v_mfma_f32_16x16x32_bf16 v[92:95], v[108:111], v[40:43], v[92:95]
	ds_read_b128 v[108:111], v164 offset:24576
	s_waitcnt lgkmcnt(7)
	v_mfma_f32_16x16x32_bf16 v[64:67], v[112:115], v[12:15], v[64:67]
	v_mfma_f32_16x16x32_bf16 v[68:71], v[112:115], v[44:47], v[68:71]
	v_xor_b32_e32 v164, 0x140, v163
	ds_read_b128 v[112:115], v164
	s_waitcnt lgkmcnt(7)
	v_mfma_f32_16x16x32_bf16 v[72:75], v[116:119], v[12:15], v[72:75]
	v_mfma_f32_16x16x32_bf16 v[76:79], v[116:119], v[44:47], v[76:79]
	ds_read_b128 v[116:119], v164 offset:8192
	s_waitcnt lgkmcnt(7)
	v_mfma_f32_16x16x32_bf16 v[80:83], v[120:123], v[12:15], v[80:83]
	v_mfma_f32_16x16x32_bf16 v[84:87], v[120:123], v[44:47], v[84:87]
	ds_read_b128 v[120:123], v164 offset:16384
	s_waitcnt lgkmcnt(7)
	v_mfma_f32_16x16x32_bf16 v[88:91], v[124:127], v[12:15], v[88:91]
	v_mfma_f32_16x16x32_bf16 v[92:95], v[124:127], v[44:47], v[92:95]
	ds_read_b128 v[124:127], v164 offset:24576
	s_waitcnt lgkmcnt(7)
	v_mfma_f32_16x16x32_bf16 v[64:67], v[96:99], v[16:19], v[64:67]
	v_mfma_f32_16x16x32_bf16 v[68:71], v[96:99], v[48:51], v[68:71]
	v_xor_b32_e32 v164, 0x180, v163
	ds_read_b128 v[96:99], v164
	s_waitcnt lgkmcnt(7)
	v_mfma_f32_16x16x32_bf16 v[72:75], v[100:103], v[16:19], v[72:75]
	v_mfma_f32_16x16x32_bf16 v[76:79], v[100:103], v[48:51], v[76:79]
	ds_read_b128 v[100:103], v164 offset:8192
	s_waitcnt lgkmcnt(7)
	v_mfma_f32_16x16x32_bf16 v[80:83], v[104:107], v[16:19], v[80:83]
	v_mfma_f32_16x16x32_bf16 v[84:87], v[104:107], v[48:51], v[84:87]
	ds_read_b128 v[104:107], v164 offset:16384
	s_waitcnt lgkmcnt(7)
	v_mfma_f32_16x16x32_bf16 v[88:91], v[108:111], v[16:19], v[88:91]
	v_mfma_f32_16x16x32_bf16 v[92:95], v[108:111], v[48:51], v[92:95]
	ds_read_b128 v[108:111], v164 offset:24576
	s_waitcnt lgkmcnt(7)
	v_mfma_f32_16x16x32_bf16 v[64:67], v[112:115], v[20:23], v[64:67]
	v_mfma_f32_16x16x32_bf16 v[68:71], v[112:115], v[52:55], v[68:71]
	v_xor_b32_e32 v164, 0x1c0, v163
	ds_read_b128 v[112:115], v164
	s_waitcnt lgkmcnt(7)
	v_mfma_f32_16x16x32_bf16 v[72:75], v[116:119], v[20:23], v[72:75]
	v_mfma_f32_16x16x32_bf16 v[76:79], v[116:119], v[52:55], v[76:79]
	ds_read_b128 v[116:119], v164 offset:8192
	s_waitcnt lgkmcnt(7)
	v_mfma_f32_16x16x32_bf16 v[80:83], v[120:123], v[20:23], v[80:83]
	v_mfma_f32_16x16x32_bf16 v[84:87], v[120:123], v[52:55], v[84:87]
	ds_read_b128 v[120:123], v164 offset:16384
	s_waitcnt lgkmcnt(7)
	v_mfma_f32_16x16x32_bf16 v[88:91], v[124:127], v[20:23], v[88:91]
	v_mfma_f32_16x16x32_bf16 v[92:95], v[124:127], v[52:55], v[92:95]
	ds_read_b128 v[124:127], v164 offset:24576
	s_waitcnt lgkmcnt(7)
	v_mfma_f32_16x16x32_bf16 v[64:67], v[96:99], v[24:27], v[64:67]
	v_mfma_f32_16x16x32_bf16 v[68:71], v[96:99], v[56:59], v[68:71]
	s_waitcnt lgkmcnt(6)
	v_mfma_f32_16x16x32_bf16 v[72:75], v[100:103], v[24:27], v[72:75]
	v_mfma_f32_16x16x32_bf16 v[76:79], v[100:103], v[56:59], v[76:79]
	s_waitcnt lgkmcnt(5)
	v_mfma_f32_16x16x32_bf16 v[80:83], v[104:107], v[24:27], v[80:83]
	v_mfma_f32_16x16x32_bf16 v[84:87], v[104:107], v[56:59], v[84:87]
	s_waitcnt lgkmcnt(4)
	v_mfma_f32_16x16x32_bf16 v[88:91], v[108:111], v[24:27], v[88:91]
	v_mfma_f32_16x16x32_bf16 v[92:95], v[108:111], v[56:59], v[92:95]
	s_waitcnt lgkmcnt(3)
	v_mfma_f32_16x16x32_bf16 v[64:67], v[112:115], v[28:31], v[64:67]
	v_mfma_f32_16x16x32_bf16 v[68:71], v[112:115], v[60:63], v[68:71]
	s_waitcnt lgkmcnt(2)
	v_mfma_f32_16x16x32_bf16 v[72:75], v[116:119], v[28:31], v[72:75]
	v_mfma_f32_16x16x32_bf16 v[76:79], v[116:119], v[60:63], v[76:79]
	s_waitcnt lgkmcnt(1)
	v_mfma_f32_16x16x32_bf16 v[80:83], v[120:123], v[28:31], v[80:83]
	v_mfma_f32_16x16x32_bf16 v[84:87], v[120:123], v[60:63], v[84:87]
	s_waitcnt lgkmcnt(0)
	v_mfma_f32_16x16x32_bf16 v[88:91], v[124:127], v[28:31], v[88:91]
	v_mfma_f32_16x16x32_bf16 v[92:95], v[124:127], v[60:63], v[92:95]
	v_or_b32_e32 v169, 0x10000, v165
	v_or_b32_e32 v170, 0x10000, v166
	v_or_b32_e32 v171, 0x10000, v167
	v_or_b32_e32 v172, 0x10000, v168
	ds_read_u16 v144, v169
	ds_read_u16 v145, v170
	ds_read_u16 v146, v171
	ds_read_u16 v147, v172
	ds_read_u16 v148, v169 offset:8192
	ds_read_u16 v149, v170 offset:8192
	ds_read_u16 v150, v171 offset:8192
	ds_read_u16 v151, v172 offset:8192
	ds_read_u16 v152, v169 offset:16384
	ds_read_u16 v153, v170 offset:16384
	ds_read_u16 v154, v171 offset:16384
	ds_read_u16 v155, v172 offset:16384
	ds_read_u16 v156, v169 offset:24576
	ds_read_u16 v157, v170 offset:24576
	ds_read_u16 v158, v171 offset:24576
	ds_read_u16 v159, v172 offset:24576
	s_nop 7
	v_fma_f32 v178, v64, s53, v173
	v_fma_f32 v179, v65, s53, v173
	v_fma_f32 v180, v66, s53, v173
	v_fma_f32 v181, v67, s53, v173
	v_fma_f32 v182, v72, s53, v173
	v_fma_f32 v183, v73, s53, v173
	v_fma_f32 v184, v74, s53, v173
	v_fma_f32 v185, v75, s53, v173
	v_fma_f32 v186, v68, s53, v174
	v_fma_f32 v187, v69, s53, v174
	v_fma_f32 v188, v70, s53, v174
	v_fma_f32 v189, v71, s53, v174
	v_fma_f32 v190, v76, s53, v174
	v_fma_f32 v191, v77, s53, v174
	v_fma_f32 v192, v78, s53, v174
	v_fma_f32 v193, v79, s53, v174
	v_exp_f32_e32 v178, v178
	v_exp_f32_e32 v179, v179
	v_exp_f32_e32 v180, v180
	v_exp_f32_e32 v181, v181
	v_exp_f32_e32 v182, v182
	v_exp_f32_e32 v183, v183
	v_exp_f32_e32 v184, v184
	v_exp_f32_e32 v185, v185
	v_exp_f32_e32 v186, v186
	v_exp_f32_e32 v187, v187
	v_exp_f32_e32 v188, v188
	v_exp_f32_e32 v189, v189
	v_exp_f32_e32 v190, v190
	v_exp_f32_e32 v191, v191
	v_exp_f32_e32 v192, v192
	v_exp_f32_e32 v193, v193
	v_add_f32_e32 v178, 1.0, v178
	v_add_f32_e32 v179, 1.0, v179
	v_add_f32_e32 v180, 1.0, v180
	v_add_f32_e32 v181, 1.0, v181
	v_add_f32_e32 v182, 1.0, v182
	v_add_f32_e32 v183, 1.0, v183
	v_add_f32_e32 v184, 1.0, v184
	v_add_f32_e32 v185, 1.0, v185
	v_add_f32_e32 v186, 1.0, v186
	v_add_f32_e32 v187, 1.0, v187
	v_add_f32_e32 v188, 1.0, v188
	v_add_f32_e32 v189, 1.0, v189
	v_add_f32_e32 v190, 1.0, v190
	v_add_f32_e32 v191, 1.0, v191
	v_add_f32_e32 v192, 1.0, v192
	v_add_f32_e32 v193, 1.0, v193
	v_rcp_f32_e32 v178, v178
	v_rcp_f32_e32 v179, v179
	v_rcp_f32_e32 v180, v180
	v_rcp_f32_e32 v181, v181
	v_rcp_f32_e32 v182, v182
	v_rcp_f32_e32 v183, v183
	v_rcp_f32_e32 v184, v184
	v_rcp_f32_e32 v185, v185
	v_rcp_f32_e32 v186, v186
	v_rcp_f32_e32 v187, v187
	v_rcp_f32_e32 v188, v188
	v_rcp_f32_e32 v189, v189
	v_rcp_f32_e32 v190, v190
	v_rcp_f32_e32 v191, v191
	v_rcp_f32_e32 v192, v192
	v_rcp_f32_e32 v193, v193
	v_mul_f32_e32 v178, v175, v178
	v_mul_f32_e32 v179, v175, v179
	v_mul_f32_e32 v180, v175, v180
	v_mul_f32_e32 v181, v175, v181
	v_mul_f32_e32 v182, v175, v182
	v_mul_f32_e32 v183, v175, v183
	v_mul_f32_e32 v184, v175, v184
	v_mul_f32_e32 v185, v175, v185
	v_exp_f32_e32 v96, v178
	v_exp_f32_e32 v97, v179
	v_exp_f32_e32 v98, v180
	v_exp_f32_e32 v99, v181
	v_exp_f32_e32 v100, v182
	v_exp_f32_e32 v101, v183
	v_exp_f32_e32 v102, v184
	v_exp_f32_e32 v103, v185
	s_nop 0
	v_fma_f32 v194, -v96, v96, 1.0
	v_fma_f32 v195, -v97, v97, 1.0
	v_fma_f32 v196, -v98, v98, 1.0
	v_fma_f32 v197, -v99, v99, 1.0
	v_fma_f32 v198, -v100, v100, 1.0
	v_fma_f32 v199, -v101, v101, 1.0
	v_fma_f32 v200, -v102, v102, 1.0
	v_fma_f32 v201, -v103, v103, 1.0
	v_max_f32_e32 v194, 0, v194
	v_max_f32_e32 v195, 0, v195
	v_max_f32_e32 v196, 0, v196
	v_max_f32_e32 v197, 0, v197
	v_max_f32_e32 v198, 0, v198
	v_max_f32_e32 v199, 0, v199
	v_max_f32_e32 v200, 0, v200
	v_max_f32_e32 v201, 0, v201
	v_sqrt_f32_e32 v194, v194
	v_sqrt_f32_e32 v195, v195
	v_sqrt_f32_e32 v196, v196
	v_sqrt_f32_e32 v197, v197
	v_sqrt_f32_e32 v198, v198
	v_sqrt_f32_e32 v199, v199
	v_sqrt_f32_e32 v200, v200
	v_sqrt_f32_e32 v201, v201
	s_waitcnt lgkmcnt(8)
	v_lshlrev_b32_e32 v144, 16, v144
	v_lshlrev_b32_e32 v145, 16, v145
	v_lshlrev_b32_e32 v146, 16, v146
	v_lshlrev_b32_e32 v147, 16, v147
	v_lshlrev_b32_e32 v148, 16, v148
	v_lshlrev_b32_e32 v149, 16, v149
	v_lshlrev_b32_e32 v150, 16, v150
	v_lshlrev_b32_e32 v151, 16, v151
	v_mul_f32_e32 v194, v194, v186
	v_mul_f32_e32 v195, v195, v187
	v_mul_f32_e32 v196, v196, v188
	v_mul_f32_e32 v197, v197, v189
	v_mul_f32_e32 v198, v198, v190
	v_mul_f32_e32 v199, v199, v191
	v_mul_f32_e32 v200, v200, v192
	v_mul_f32_e32 v201, v201, v193
	v_mul_f32_e32 v144, v194, v144
	v_mul_f32_e32 v145, v195, v145
	v_mul_f32_e32 v146, v196, v146
	v_mul_f32_e32 v147, v197, v147
	v_mul_f32_e32 v148, v198, v148
	v_mul_f32_e32 v149, v199, v149
	v_mul_f32_e32 v150, v200, v150
	v_mul_f32_e32 v151, v201, v151
	v_fma_f32 v178, v80, s53, v173
	v_fma_f32 v179, v81, s53, v173
	v_fma_f32 v180, v82, s53, v173
	v_fma_f32 v181, v83, s53, v173
	v_fma_f32 v182, v88, s53, v173
	v_fma_f32 v183, v89, s53, v173
	v_fma_f32 v184, v90, s53, v173
	v_fma_f32 v185, v91, s53, v173
	v_fma_f32 v186, v84, s53, v174
	v_fma_f32 v187, v85, s53, v174
	v_fma_f32 v188, v86, s53, v174
	v_fma_f32 v189, v87, s53, v174
	v_fma_f32 v190, v92, s53, v174
	v_fma_f32 v191, v93, s53, v174
	v_fma_f32 v192, v94, s53, v174
	v_fma_f32 v193, v95, s53, v174
	v_exp_f32_e32 v178, v178
	v_exp_f32_e32 v179, v179
	v_exp_f32_e32 v180, v180
	v_exp_f32_e32 v181, v181
	v_exp_f32_e32 v182, v182
	v_exp_f32_e32 v183, v183
	v_exp_f32_e32 v184, v184
	v_exp_f32_e32 v185, v185
	v_exp_f32_e32 v186, v186
	v_exp_f32_e32 v187, v187
	v_exp_f32_e32 v188, v188
	v_exp_f32_e32 v189, v189
	v_exp_f32_e32 v190, v190
	v_exp_f32_e32 v191, v191
	v_exp_f32_e32 v192, v192
	v_exp_f32_e32 v193, v193
	v_add_f32_e32 v178, 1.0, v178
	v_add_f32_e32 v179, 1.0, v179
	v_add_f32_e32 v180, 1.0, v180
	v_add_f32_e32 v181, 1.0, v181
	v_add_f32_e32 v182, 1.0, v182
	v_add_f32_e32 v183, 1.0, v183
	v_add_f32_e32 v184, 1.0, v184
	v_add_f32_e32 v185, 1.0, v185
	v_add_f32_e32 v186, 1.0, v186
	v_add_f32_e32 v187, 1.0, v187
	v_add_f32_e32 v188, 1.0, v188
	v_add_f32_e32 v189, 1.0, v189
	v_add_f32_e32 v190, 1.0, v190
	v_add_f32_e32 v191, 1.0, v191
	v_add_f32_e32 v192, 1.0, v192
	v_add_f32_e32 v193, 1.0, v193
	v_rcp_f32_e32 v178, v178
	v_rcp_f32_e32 v179, v179
	v_rcp_f32_e32 v180, v180
	v_rcp_f32_e32 v181, v181
	v_rcp_f32_e32 v182, v182
	v_rcp_f32_e32 v183, v183
	v_rcp_f32_e32 v184, v184
	v_rcp_f32_e32 v185, v185
	v_rcp_f32_e32 v186, v186
	v_rcp_f32_e32 v187, v187
	v_rcp_f32_e32 v188, v188
	v_rcp_f32_e32 v189, v189
	v_rcp_f32_e32 v190, v190
	v_rcp_f32_e32 v191, v191
	v_rcp_f32_e32 v192, v192
	v_rcp_f32_e32 v193, v193
	v_mul_f32_e32 v178, v175, v178
	v_mul_f32_e32 v179, v175, v179
	v_mul_f32_e32 v180, v175, v180
	v_mul_f32_e32 v181, v175, v181
	v_mul_f32_e32 v182, v175, v182
	v_mul_f32_e32 v183, v175, v183
	v_mul_f32_e32 v184, v175, v184
	v_mul_f32_e32 v185, v175, v185
	v_exp_f32_e32 v104, v178
	v_exp_f32_e32 v105, v179
	v_exp_f32_e32 v106, v180
	v_exp_f32_e32 v107, v181
	v_exp_f32_e32 v108, v182
	v_exp_f32_e32 v109, v183
	v_exp_f32_e32 v110, v184
	v_exp_f32_e32 v111, v185
	s_nop 0
	v_fma_f32 v194, -v104, v104, 1.0
	v_fma_f32 v195, -v105, v105, 1.0
	v_fma_f32 v196, -v106, v106, 1.0
	v_fma_f32 v197, -v107, v107, 1.0
	v_fma_f32 v198, -v108, v108, 1.0
	v_fma_f32 v199, -v109, v109, 1.0
	v_fma_f32 v200, -v110, v110, 1.0
	v_fma_f32 v201, -v111, v111, 1.0
	v_max_f32_e32 v194, 0, v194
	v_max_f32_e32 v195, 0, v195
	v_max_f32_e32 v196, 0, v196
	v_max_f32_e32 v197, 0, v197
	v_max_f32_e32 v198, 0, v198
	v_max_f32_e32 v199, 0, v199
	v_max_f32_e32 v200, 0, v200
	v_max_f32_e32 v201, 0, v201
	v_sqrt_f32_e32 v194, v194
	v_sqrt_f32_e32 v195, v195
	v_sqrt_f32_e32 v196, v196
	v_sqrt_f32_e32 v197, v197
	v_sqrt_f32_e32 v198, v198
	v_sqrt_f32_e32 v199, v199
	v_sqrt_f32_e32 v200, v200
	v_sqrt_f32_e32 v201, v201
	s_waitcnt lgkmcnt(0)
	v_lshlrev_b32_e32 v152, 16, v152
	v_lshlrev_b32_e32 v153, 16, v153
	v_lshlrev_b32_e32 v154, 16, v154
	v_lshlrev_b32_e32 v155, 16, v155
	v_lshlrev_b32_e32 v156, 16, v156
	v_lshlrev_b32_e32 v157, 16, v157
	v_lshlrev_b32_e32 v158, 16, v158
	v_lshlrev_b32_e32 v159, 16, v159
	v_mul_f32_e32 v194, v194, v186
	v_mul_f32_e32 v195, v195, v187
	v_mul_f32_e32 v196, v196, v188
	v_mul_f32_e32 v197, v197, v189
	v_mul_f32_e32 v198, v198, v190
	v_mul_f32_e32 v199, v199, v191
	v_mul_f32_e32 v200, v200, v192
	v_mul_f32_e32 v201, v201, v193
	v_mul_f32_e32 v152, v194, v152
	v_mul_f32_e32 v153, v195, v153
	v_mul_f32_e32 v154, v196, v154
	v_mul_f32_e32 v155, v197, v155
	v_mul_f32_e32 v156, v198, v156
	v_mul_f32_e32 v157, v199, v157
	v_mul_f32_e32 v158, v200, v158
	v_mul_f32_e32 v159, v201, v159
	v_fma_f32 v146, v98, v147, v146
	v_fma_f32 v150, v102, v151, v150
	v_fma_f32 v154, v106, v155, v154
	v_fma_f32 v158, v110, v159, v158
	v_mul_f32_e32 v98, v98, v99
	v_mul_f32_e32 v102, v102, v103
	v_mul_f32_e32 v106, v106, v107
	v_mul_f32_e32 v110, v110, v111
	v_fma_f32 v145, v97, v146, v145
	v_fma_f32 v149, v101, v150, v149
	v_fma_f32 v153, v105, v154, v153
	v_fma_f32 v157, v109, v158, v157
	v_mul_f32_e32 v97, v97, v98
	v_mul_f32_e32 v101, v101, v102
	v_mul_f32_e32 v105, v105, v106
	v_mul_f32_e32 v109, v109, v110
	v_fma_f32 v144, v96, v145, v144
	v_fma_f32 v148, v100, v149, v148
	v_fma_f32 v152, v104, v153, v152
	v_fma_f32 v156, v108, v157, v156
	v_mul_f32_e32 v96, v96, v97
	v_mul_f32_e32 v100, v100, v101
	v_mul_f32_e32 v104, v104, v105
	v_mul_f32_e32 v108, v108, v109
	ds_bpermute_b32 v178, v204, v96
	ds_bpermute_b32 v182, v204, v144
	ds_bpermute_b32 v179, v204, v100
	ds_bpermute_b32 v183, v204, v148
	ds_bpermute_b32 v180, v204, v104
	ds_bpermute_b32 v184, v204, v152
	ds_bpermute_b32 v181, v204, v108
	ds_bpermute_b32 v185, v204, v156
	s_waitcnt lgkmcnt(0)
	v_fma_f32 v186, v182, v96, v144
	v_cndmask_b32_e64 v178, 1.0, v178, s[34:35]
	v_fma_f32 v187, v183, v100, v148
	v_cndmask_b32_e64 v179, 1.0, v179, s[34:35]
	v_fma_f32 v188, v184, v104, v152
	v_cndmask_b32_e64 v180, 1.0, v180, s[34:35]
	v_fma_f32 v189, v185, v108, v156
	v_cndmask_b32_e64 v181, 1.0, v181, s[34:35]
	v_cndmask_b32_e64 v223, v144, v186, s[34:35]
	v_mul_f32_e32 v219, v96, v178
	v_cndmask_b32_e64 v224, v148, v187, s[34:35]
	v_mul_f32_e32 v220, v100, v179
	v_cndmask_b32_e64 v225, v152, v188, s[34:35]
	v_mul_f32_e32 v221, v104, v180
	v_cndmask_b32_e64 v226, v156, v189, s[34:35]
	v_mul_f32_e32 v222, v108, v181
	ds_bpermute_b32 v178, v205, v219
	ds_bpermute_b32 v182, v205, v223
	ds_bpermute_b32 v179, v205, v220
	ds_bpermute_b32 v183, v205, v224
	ds_bpermute_b32 v180, v205, v221
	ds_bpermute_b32 v184, v205, v225
	ds_bpermute_b32 v181, v205, v222
	ds_bpermute_b32 v185, v205, v226
	s_waitcnt lgkmcnt(0)
	v_fma_f32 v186, v182, v219, v223
	v_cndmask_b32_e64 v178, 1.0, v178, s[36:37]
	v_fma_f32 v187, v183, v220, v224
	v_cndmask_b32_e64 v179, 1.0, v179, s[36:37]
	v_fma_f32 v188, v184, v221, v225
	v_cndmask_b32_e64 v180, 1.0, v180, s[36:37]
	v_fma_f32 v189, v185, v222, v226
	v_cndmask_b32_e64 v181, 1.0, v181, s[36:37]
	v_cndmask_b32_e64 v223, v223, v186, s[36:37]
	v_mul_f32_e32 v219, v219, v178
	v_cndmask_b32_e64 v224, v224, v187, s[36:37]
	v_mul_f32_e32 v220, v220, v179
	v_cndmask_b32_e64 v225, v225, v188, s[36:37]
	v_mul_f32_e32 v221, v221, v180
	v_cndmask_b32_e64 v226, v226, v189, s[36:37]
	v_mul_f32_e32 v222, v222, v181
	ds_bpermute_b32 v227, v204, v219
	ds_bpermute_b32 v231, v204, v223
	ds_bpermute_b32 v235, v206, v219
	ds_bpermute_b32 v239, v206, v223
	ds_bpermute_b32 v228, v204, v220
	ds_bpermute_b32 v232, v204, v224
	ds_bpermute_b32 v236, v206, v220
	ds_bpermute_b32 v244, v206, v224
	ds_bpermute_b32 v229, v204, v221
	ds_bpermute_b32 v233, v204, v225
	ds_bpermute_b32 v237, v206, v221
	ds_bpermute_b32 v245, v206, v225
	ds_bpermute_b32 v230, v204, v222
	ds_bpermute_b32 v234, v204, v226
	ds_bpermute_b32 v238, v206, v222
	ds_bpermute_b32 v246, v206, v226
	s_waitcnt lgkmcnt(0)
	v_cndmask_b32_e64 v227, 1.0, v227, s[34:35]
	v_cndmask_b32_e64 v231, 0, v231, s[34:35]
	v_cndmask_b32_e64 v228, 1.0, v228, s[34:35]
	v_cndmask_b32_e64 v232, 0, v232, s[34:35]
	v_cndmask_b32_e64 v229, 1.0, v229, s[34:35]
	v_cndmask_b32_e64 v233, 0, v233, s[34:35]
	v_cndmask_b32_e64 v230, 1.0, v230, s[34:35]
	v_cndmask_b32_e64 v234, 0, v234, s[34:35]
	v_mov_b32_e32 v190, v238
	v_mov_b32_e32 v194, v246
	v_mov_b32_e32 v198, v190
	v_mov_b32_e32 v201, v194
	v_fma_f32 v194, v194, v237, v245
	v_mul_f32_e32 v190, v190, v237
	v_mov_b32_e32 v199, v190
	v_mov_b32_e32 v177, v194
	v_fma_f32 v194, v194, v236, v244
	v_mul_f32_e32 v190, v190, v236
	v_mov_b32_e32 v200, v190
	v_mov_b32_e32 v203, v194
	v_fma_f32 v194, v194, v235, v239
	v_mul_f32_e32 v190, v190, v235
	v_mov_b32_e32 v191, v194
	ds_write_b64 v207, v[190:191] offset:1024
	s_cmp_eq_u32 s13, 17
	s_cbranch_scc1 .Lmylru_g0_10
	s_waitcnt vmcnt(8)
	s_branch .Lmylru_g1_10

.Lmylru_g1_10:
	s_waitcnt lgkmcnt(0)
	s_barrier
	ds_read_b64 v[178:179], v208 offset:1536
	ds_read_b64 v[180:181], v208 offset:1024
	s_waitcnt lgkmcnt(0)
	v_fma_f32 v182, v176, v178, v179
	v_cndmask_b32_e64 v183, v176, v182, s[38:39]
	v_fma_f32 v176, v182, v180, v181
	v_fma_f32 v184, v183, v200, v203
	v_fma_f32 v185, v183, v199, v177
	v_fma_f32 v186, v183, v198, v201
	v_mov_b32_e32 v187, v183
	v_fma_f32 v184, v184, v227, v231
	v_fma_f32 v185, v185, v228, v232
	v_fma_f32 v186, v186, v229, v233
	v_fma_f32 v187, v187, v230, v234
	v_fma_f32 v144, v184, v96, v144
	v_fma_f32 v148, v185, v100, v148
	v_fma_f32 v152, v186, v104, v152
	v_fma_f32 v156, v187, v108, v156
	v_fma_f32 v145, v184, v97, v145
	v_fma_f32 v149, v185, v101, v149
	v_fma_f32 v153, v186, v105, v153
	v_fma_f32 v157, v187, v109, v157
	v_fma_f32 v146, v184, v98, v146
	v_fma_f32 v150, v185, v102, v150
	v_fma_f32 v154, v186, v106, v154
	v_fma_f32 v158, v187, v110, v158
	v_fma_f32 v147, v184, v99, v147
	v_fma_f32 v151, v185, v103, v151
	v_fma_f32 v155, v186, v107, v155
	v_fma_f32 v159, v187, v111, v159
	s_cmp_eq_u32 s13, 17
	s_cbranch_scc1 .Lmylru_w0_9
	s_waitcnt vmcnt(8)
	s_branch .Lmylru_w1_9

.Lmylru_w1_9:
	v_lshrrev_b32_e32 v184, 11, v210
	v_and_b32_e32 v185, 0x7ff, v210
	v_lshl_add_u32 v184, v184, 7, v185
	v_add_u32_e32 v184, 0x20800, v184
	ds_read_u16 v128, v184
	ds_read_u16 v129, v184 offset:128
	ds_read_u16 v130, v184 offset:256
	ds_read_u16 v131, v184 offset:384
	ds_read_u16 v132, v184 offset:2048
	ds_read_u16 v133, v184 offset:2176
	ds_read_u16 v134, v184 offset:2304
	ds_read_u16 v135, v184 offset:2432
	ds_read_u16 v136, v184 offset:4096
	ds_read_u16 v137, v184 offset:4224
	ds_read_u16 v138, v184 offset:4352
	ds_read_u16 v139, v184 offset:4480
	ds_read_u16 v140, v184 offset:6144
	ds_read_u16 v141, v184 offset:6272
	ds_read_u16 v142, v184 offset:6400
	ds_read_u16 v143, v184 offset:6528
	s_waitcnt lgkmcnt(0)
	v_lshlrev_b32_e32 v178, 16, v247
	v_add_f32_e32 v144, v144, v178
	v_lshlrev_b32_e32 v128, 16, v128
	v_mul_f32_e32 v144, v144, v128
	v_cvt_pk_bf16_f32 v144, v144, v144
	v_and_b32_e32 v179, 0xffff0000, v247
	v_add_f32_e32 v145, v145, v179
	v_lshlrev_b32_e32 v129, 16, v129
	v_mul_f32_e32 v145, v145, v129
	v_cvt_pk_bf16_f32 v145, v145, v145
	v_lshlrev_b32_e32 v180, 16, v248
	v_add_f32_e32 v146, v146, v180
	v_lshlrev_b32_e32 v130, 16, v130
	v_mul_f32_e32 v146, v146, v130
	v_cvt_pk_bf16_f32 v146, v146, v146
	v_and_b32_e32 v181, 0xffff0000, v248
	v_add_f32_e32 v147, v147, v181
	v_lshlrev_b32_e32 v131, 16, v131
	v_mul_f32_e32 v147, v147, v131
	v_cvt_pk_bf16_f32 v147, v147, v147
	v_lshlrev_b32_e32 v178, 16, v249
	v_add_f32_e32 v148, v148, v178
	v_lshlrev_b32_e32 v132, 16, v132
	v_mul_f32_e32 v148, v148, v132
	v_cvt_pk_bf16_f32 v148, v148, v148
	v_and_b32_e32 v179, 0xffff0000, v249
	v_add_f32_e32 v149, v149, v179
	v_lshlrev_b32_e32 v133, 16, v133
	v_mul_f32_e32 v149, v149, v133
	v_cvt_pk_bf16_f32 v149, v149, v149
	v_lshlrev_b32_e32 v180, 16, v250
	v_add_f32_e32 v150, v150, v180
	v_lshlrev_b32_e32 v134, 16, v134
	v_mul_f32_e32 v150, v150, v134
	v_cvt_pk_bf16_f32 v150, v150, v150
	v_and_b32_e32 v181, 0xffff0000, v250
	v_add_f32_e32 v151, v151, v181
	v_lshlrev_b32_e32 v135, 16, v135
	v_mul_f32_e32 v151, v151, v135
	v_cvt_pk_bf16_f32 v151, v151, v151
	v_lshlrev_b32_e32 v178, 16, v251
	v_add_f32_e32 v152, v152, v178
	v_lshlrev_b32_e32 v136, 16, v136
	v_mul_f32_e32 v152, v152, v136
	v_cvt_pk_bf16_f32 v152, v152, v152
	v_and_b32_e32 v179, 0xffff0000, v251
	v_add_f32_e32 v153, v153, v179
	v_lshlrev_b32_e32 v137, 16, v137
	v_mul_f32_e32 v153, v153, v137
	v_cvt_pk_bf16_f32 v153, v153, v153
	v_lshlrev_b32_e32 v180, 16, v252
	v_add_f32_e32 v154, v154, v180
	v_lshlrev_b32_e32 v138, 16, v138
	v_mul_f32_e32 v154, v154, v138
	v_cvt_pk_bf16_f32 v154, v154, v154
	v_and_b32_e32 v181, 0xffff0000, v252
	v_add_f32_e32 v155, v155, v181
	v_lshlrev_b32_e32 v139, 16, v139
	v_mul_f32_e32 v155, v155, v139
	v_cvt_pk_bf16_f32 v155, v155, v155
	v_lshlrev_b32_e32 v178, 16, v253
	v_add_f32_e32 v156, v156, v178
	v_lshlrev_b32_e32 v140, 16, v140
	v_mul_f32_e32 v156, v156, v140
	v_cvt_pk_bf16_f32 v156, v156, v156
	v_and_b32_e32 v179, 0xffff0000, v253
	v_add_f32_e32 v157, v157, v179
	v_lshlrev_b32_e32 v141, 16, v141
	v_mul_f32_e32 v157, v157, v141
	v_cvt_pk_bf16_f32 v157, v157, v157
	v_lshlrev_b32_e32 v180, 16, v254
	v_add_f32_e32 v158, v158, v180
	v_lshlrev_b32_e32 v142, 16, v142
	v_mul_f32_e32 v158, v158, v142
	v_cvt_pk_bf16_f32 v158, v158, v158
	v_and_b32_e32 v181, 0xffff0000, v254
	v_add_f32_e32 v159, v159, v181
	v_lshlrev_b32_e32 v143, 16, v143
	v_mul_f32_e32 v159, v159, v143
	v_cvt_pk_bf16_f32 v159, v159, v159
	v_add_u32_e32 v182, 0x0, v210
	v_add_u32_e32 v183, 0x1000, v182
	global_store_short v182, v144, s[42:43]
	global_store_short v182, v145, s[42:43] offset:2048
	global_store_short v183, v146, s[42:43]
	global_store_short v183, v147, s[42:43] offset:2048
	v_add_u32_e32 v182, 0x8000, v210
	v_add_u32_e32 v183, 0x1000, v182
	global_store_short v182, v148, s[42:43]
	global_store_short v182, v149, s[42:43] offset:2048
	global_store_short v183, v150, s[42:43]
	global_store_short v183, v151, s[42:43] offset:2048
	v_add_u32_e32 v182, 0x10000, v210
	v_add_u32_e32 v183, 0x1000, v182
	global_store_short v182, v152, s[42:43]
	global_store_short v182, v153, s[42:43] offset:2048
	global_store_short v183, v154, s[42:43]
	global_store_short v183, v155, s[42:43] offset:2048
	v_add_u32_e32 v182, 0x18000, v210
	v_add_u32_e32 v183, 0x1000, v182
	global_store_short v182, v156, s[42:43]
	global_store_short v182, v157, s[42:43] offset:2048
	global_store_short v183, v158, s[42:43]
	global_store_short v183, v159, s[42:43] offset:2048
	s_add_i32 s13, s13, 1
	s_add_i32 s60, s60, -1
	s_cmp_lg_u32 s60, 0
	s_cbranch_scc1 .Lmylru_loop_1
	s_waitcnt vmcnt(0) lgkmcnt(0)
